# P8 router: operand lookahead three chunks (four register buffers) instead of two
# speedup vs baseline: 1.0005x; 1.0005x over previous
; __device__ __forceinline__ float bf_lo(unsigned w) { return __uint_as_float(w << 16); }
; __device__ __forceinline__ float bf_hi(unsigned w) { return __uint_as_float(w & 0xffff0000u); }
; __global__ void __launch_bounds__(512, 2) fwd_kernel(Params p) {
;     ...
;             if (tid < 32) hist[tid] = 0;
;             {
;                 const bf16_t* xr = X1 + (size_t)(blk * 64 + tt * 32 + j) * DM + kq * 512 + hh * 4;
;                 const float* wr_ = WrT + (size_t)j * DM + kq * 512 + hh * 4;
;                 f32x16 acc = {}; float ss = 0.f;
;                 u32x2 xb[2][8]; f32x4 wb[2][8];
; #pragma unroll
;                 for (int i = 0; i < 8; ++i) { xb[0][i] = *(const u32x2*)(xr + i * 8); wb[0][i] = *(const f32x4*)(wr_ + i * 8); }
; #pragma unroll
;                 for (int ch = 0; ch < 8; ++ch) {
;                     if (ch + 1 < 8) {
; #pragma unroll
;                         for (int i = 0; i < 8; ++i) { xb[(ch + 1) & 1][i] = *(const u32x2*)(xr + (ch + 1) * 64 + i * 8); wb[(ch + 1) & 1][i] = *(const f32x4*)(wr_ + (ch + 1) * 64 + i * 8); } }
; #pragma unroll
;                     for (int i = 0; i < 8; ++i) { const u32x2 xp = xb[ch & 1][i]; const f32x4 xv = {bf_lo(xp.x), bf_hi(xp.x), bf_lo(xp.y), bf_hi(xp.y)}, wv = wb[ch & 1][i];
;                         acc = __builtin_amdgcn_mfma_f32_32x32x2f32(wv.x, xv.x, acc, 0, 0, 0); acc = __builtin_amdgcn_mfma_f32_32x32x2f32(wv.y, xv.y, acc, 0, 0, 0);
;                         acc = __builtin_amdgcn_mfma_f32_32x32x2f32(wv.z, xv.z, acc, 0, 0, 0); acc = __builtin_amdgcn_mfma_f32_32x32x2f32(wv.w, xv.w, acc, 0, 0, 0);
;                         ss += (xv.x * xv.x + xv.y * xv.y) + (xv.z * xv.z + xv.w * xv.w); }
.LBB0_982:
	s_and_saveexec_b64 s[10:11], s[4:5]
	ds_write_b32 v132, v87 offset:53760
	s_or_b64 exec, exec, s[10:11]
	s_lshl_b32 s10, s78, 6
	v_or_b32_e32 v0, s10, v133
	v_ashrrev_i32_e32 v1, 31, v0
	v_lshlrev_b64 v[0:1], 12, v[0:1]
	v_lshl_add_u64 v[98:99], v[88:89], 0, v[0:1]
	v_mbcnt_lo_u32_b32 v140, -1, 0
	v_mbcnt_hi_u32_b32 v140, -1, v140
	v_lshrrev_b32_e32 v140, 5, v140
	v_mov_b32_e32 v143, 0
	v_lshlrev_b32_e32 v142, 3, v140
	v_lshl_add_u64 v[100:101], v[98:99], 0, v[142:143]
	v_lshlrev_b32_e32 v142, 4, v140
	v_lshl_add_u64 v[102:103], v[90:91], 0, v[142:143]
	v_mov_b32_e32 v99, 0
	global_load_dwordx4 v[148:151], v[100:101], off
	global_load_dwordx4 v[152:155], v[102:103], off
	global_load_dwordx4 v[156:159], v[102:103], off offset:16
	global_load_dwordx4 v[160:163], v[100:101], off offset:32
	global_load_dwordx4 v[164:167], v[102:103], off offset:64
	global_load_dwordx4 v[168:171], v[102:103], off offset:80
	global_load_dwordx4 v[172:175], v[100:101], off offset:64
	global_load_dwordx4 v[176:179], v[102:103], off offset:128
	global_load_dwordx4 v[180:183], v[102:103], off offset:144
	global_load_dwordx4 v[184:187], v[100:101], off offset:96
	global_load_dwordx4 v[188:191], v[102:103], off offset:192
	global_load_dwordx4 v[192:195], v[102:103], off offset:208
	global_load_dwordx4 v[196:199], v[100:101], off offset:128
	global_load_dwordx4 v[200:203], v[102:103], off offset:256
	global_load_dwordx4 v[204:207], v[102:103], off offset:272
	global_load_dwordx4 v[208:211], v[100:101], off offset:160
	global_load_dwordx4 v[212:215], v[102:103], off offset:320
	global_load_dwordx4 v[216:219], v[102:103], off offset:336
	global_load_dwordx4 v[220:223], v[100:101], off offset:192
	global_load_dwordx4 v[224:227], v[102:103], off offset:384
	global_load_dwordx4 v[228:231], v[102:103], off offset:400
	global_load_dwordx4 v[232:235], v[100:101], off offset:224
	global_load_dwordx4 v[236:239], v[102:103], off offset:448
	global_load_dwordx4 v[240:243], v[102:103], off offset:464
	global_load_dwordx4 v[16:19], v[100:101], off offset:256
	global_load_dwordx4 v[20:23], v[102:103], off offset:512
	global_load_dwordx4 v[24:27], v[102:103], off offset:528
	global_load_dwordx4 v[28:31], v[100:101], off offset:288
	global_load_dwordx4 v[32:35], v[102:103], off offset:576
	global_load_dwordx4 v[36:39], v[102:103], off offset:592
	global_load_dwordx4 v[40:43], v[100:101], off offset:320
	global_load_dwordx4 v[44:47], v[102:103], off offset:640
	global_load_dwordx4 v[48:51], v[102:103], off offset:656
	global_load_dwordx4 v[52:55], v[100:101], off offset:352
	global_load_dwordx4 v[56:59], v[102:103], off offset:704
	global_load_dwordx4 v[60:63], v[102:103], off offset:720
	global_load_dwordx4 v[64:67], v[100:101], off offset:384
	global_load_dwordx4 v[68:71], v[102:103], off offset:768
	global_load_dwordx4 v[72:75], v[102:103], off offset:784
	global_load_dwordx4 v[76:79], v[100:101], off offset:416
	global_load_dwordx4 v[80:83], v[102:103], off offset:832
	global_load_dwordx4 v[104:107], v[102:103], off offset:848
	global_load_dwordx4 v[108:111], v[100:101], off offset:448
	global_load_dwordx4 v[112:115], v[102:103], off offset:896
	global_load_dwordx4 v[116:119], v[102:103], off offset:912
	global_load_dwordx4 v[120:123], v[100:101], off offset:480
	global_load_dwordx4 v[124:127], v[102:103], off offset:960
	global_load_dwordx4 v[128:131], v[102:103], off offset:976
	s_waitcnt vmcnt(45)
	v_lshlrev_b32_e32 v140, 16, v148
	v_and_b32_e32 v141, 0xffff0000, v148
	v_lshlrev_b32_e32 v142, 16, v149
	v_and_b32_e32 v143, 0xffff0000, v149
	v_lshlrev_b32_e32 v144, 16, v150
	v_and_b32_e32 v145, 0xffff0000, v150
	v_lshlrev_b32_e32 v146, 16, v151
	v_and_b32_e32 v147, 0xffff0000, v151
	s_waitcnt vmcnt(42)
	v_mfma_f32_32x32x2_f32 v[0:15], v152, v140, 0
	v_lshlrev_b32_e32 v244, 16, v160
	v_fmac_f32_e32 v99, v140, v140
	v_mfma_f32_32x32x2_f32 v[0:15], v153, v141, v[0:15]
	v_and_b32_e32 v245, 0xffff0000, v160
	v_fmac_f32_e32 v99, v141, v141
	v_mfma_f32_32x32x2_f32 v[0:15], v154, v142, v[0:15]
	v_lshlrev_b32_e32 v246, 16, v161
	v_fmac_f32_e32 v99, v142, v142
	v_mfma_f32_32x32x2_f32 v[0:15], v155, v143, v[0:15]
	v_and_b32_e32 v247, 0xffff0000, v161
	v_fmac_f32_e32 v99, v143, v143
	v_mfma_f32_32x32x2_f32 v[0:15], v156, v144, v[0:15]
	v_lshlrev_b32_e32 v248, 16, v162
	v_fmac_f32_e32 v99, v144, v144
	v_mfma_f32_32x32x2_f32 v[0:15], v157, v145, v[0:15]
	v_and_b32_e32 v249, 0xffff0000, v162
	v_fmac_f32_e32 v99, v145, v145
	v_mfma_f32_32x32x2_f32 v[0:15], v158, v146, v[0:15]
	v_lshlrev_b32_e32 v250, 16, v163
	v_fmac_f32_e32 v99, v146, v146
	v_mfma_f32_32x32x2_f32 v[0:15], v159, v147, v[0:15]
	v_and_b32_e32 v251, 0xffff0000, v163
	v_fmac_f32_e32 v99, v147, v147
	s_waitcnt vmcnt(39)
	v_mfma_f32_32x32x2_f32 v[0:15], v164, v244, v[0:15]
	v_lshlrev_b32_e32 v140, 16, v172
	v_fmac_f32_e32 v99, v244, v244
	v_mfma_f32_32x32x2_f32 v[0:15], v165, v245, v[0:15]
	v_and_b32_e32 v141, 0xffff0000, v172
	v_fmac_f32_e32 v99, v245, v245
	v_mfma_f32_32x32x2_f32 v[0:15], v166, v246, v[0:15]
	v_lshlrev_b32_e32 v142, 16, v173
	v_fmac_f32_e32 v99, v246, v246
	v_mfma_f32_32x32x2_f32 v[0:15], v167, v247, v[0:15]
	v_and_b32_e32 v143, 0xffff0000, v173
	v_fmac_f32_e32 v99, v247, v247
	v_mfma_f32_32x32x2_f32 v[0:15], v168, v248, v[0:15]
	v_lshlrev_b32_e32 v144, 16, v174
	v_fmac_f32_e32 v99, v248, v248
	v_mfma_f32_32x32x2_f32 v[0:15], v169, v249, v[0:15]
	v_and_b32_e32 v145, 0xffff0000, v174
	v_fmac_f32_e32 v99, v249, v249
	v_mfma_f32_32x32x2_f32 v[0:15], v170, v250, v[0:15]
	v_lshlrev_b32_e32 v146, 16, v175
	v_fmac_f32_e32 v99, v250, v250
	v_mfma_f32_32x32x2_f32 v[0:15], v171, v251, v[0:15]
	v_and_b32_e32 v147, 0xffff0000, v175
	v_fmac_f32_e32 v99, v251, v251
	s_waitcnt vmcnt(36)
; __device__ __forceinline__ float bf_lo(unsigned w) { return __uint_as_float(w << 16); }
; __device__ __forceinline__ float bf_hi(unsigned w) { return __uint_as_float(w & 0xffff0000u); }
; __global__ void __launch_bounds__(512, 2) fwd_kernel(Params p) {
;     ...
;                 for (int ch = 0; ch < 8; ++ch) {
;                     if (ch + 1 < 8) {
; #pragma unroll
;                         for (int i = 0; i < 8; ++i) { xb[(ch + 1) & 1][i] = *(const u32x2*)(xr + (ch + 1) * 64 + i * 8); wb[(ch + 1) & 1][i] = *(const f32x4*)(wr_ + (ch + 1) * 64 + i * 8); } }
; #pragma unroll
;                     for (int i = 0; i < 8; ++i) { const u32x2 xp = xb[ch & 1][i]; const f32x4 xv = {bf_lo(xp.x), bf_hi(xp.x), bf_lo(xp.y), bf_hi(xp.y)}, wv = wb[ch & 1][i];
;                         acc = __builtin_amdgcn_mfma_f32_32x32x2f32(wv.x, xv.x, acc, 0, 0, 0); acc = __builtin_amdgcn_mfma_f32_32x32x2f32(wv.y, xv.y, acc, 0, 0, 0);
;                         acc = __builtin_amdgcn_mfma_f32_32x32x2f32(wv.z, xv.z, acc, 0, 0, 0); acc = __builtin_amdgcn_mfma_f32_32x32x2f32(wv.w, xv.w, acc, 0, 0, 0);
;                         ss += (xv.x * xv.x + xv.y * xv.y) + (xv.z * xv.z + xv.w * xv.w); }
	v_mfma_f32_32x32x2_f32 v[0:15], v176, v140, v[0:15]
	v_lshlrev_b32_e32 v244, 16, v184
	v_fmac_f32_e32 v99, v140, v140
	v_mfma_f32_32x32x2_f32 v[0:15], v177, v141, v[0:15]
	v_and_b32_e32 v245, 0xffff0000, v184
	v_fmac_f32_e32 v99, v141, v141
	v_mfma_f32_32x32x2_f32 v[0:15], v178, v142, v[0:15]
	v_lshlrev_b32_e32 v246, 16, v185
	v_fmac_f32_e32 v99, v142, v142
	v_mfma_f32_32x32x2_f32 v[0:15], v179, v143, v[0:15]
	v_and_b32_e32 v247, 0xffff0000, v185
	v_fmac_f32_e32 v99, v143, v143
	v_mfma_f32_32x32x2_f32 v[0:15], v180, v144, v[0:15]
	v_lshlrev_b32_e32 v248, 16, v186
	v_fmac_f32_e32 v99, v144, v144
	v_mfma_f32_32x32x2_f32 v[0:15], v181, v145, v[0:15]
	v_and_b32_e32 v249, 0xffff0000, v186
	v_fmac_f32_e32 v99, v145, v145
	v_mfma_f32_32x32x2_f32 v[0:15], v182, v146, v[0:15]
	v_lshlrev_b32_e32 v250, 16, v187
	v_fmac_f32_e32 v99, v146, v146
	v_mfma_f32_32x32x2_f32 v[0:15], v183, v147, v[0:15]
	v_and_b32_e32 v251, 0xffff0000, v187
	v_fmac_f32_e32 v99, v147, v147
	s_waitcnt vmcnt(33)
	v_mfma_f32_32x32x2_f32 v[0:15], v188, v244, v[0:15]
	v_lshlrev_b32_e32 v140, 16, v196
	v_fmac_f32_e32 v99, v244, v244
	v_mfma_f32_32x32x2_f32 v[0:15], v189, v245, v[0:15]
	v_and_b32_e32 v141, 0xffff0000, v196
	v_fmac_f32_e32 v99, v245, v245
	v_mfma_f32_32x32x2_f32 v[0:15], v190, v246, v[0:15]
	v_lshlrev_b32_e32 v142, 16, v197
	v_fmac_f32_e32 v99, v246, v246
	v_mfma_f32_32x32x2_f32 v[0:15], v191, v247, v[0:15]
	v_and_b32_e32 v143, 0xffff0000, v197
	v_fmac_f32_e32 v99, v247, v247
	v_mfma_f32_32x32x2_f32 v[0:15], v192, v248, v[0:15]
	v_lshlrev_b32_e32 v144, 16, v198
	v_fmac_f32_e32 v99, v248, v248
	v_mfma_f32_32x32x2_f32 v[0:15], v193, v249, v[0:15]
	v_and_b32_e32 v145, 0xffff0000, v198
	v_fmac_f32_e32 v99, v249, v249
	v_mfma_f32_32x32x2_f32 v[0:15], v194, v250, v[0:15]
	v_lshlrev_b32_e32 v146, 16, v199
	v_fmac_f32_e32 v99, v250, v250
	v_mfma_f32_32x32x2_f32 v[0:15], v195, v251, v[0:15]
	v_and_b32_e32 v147, 0xffff0000, v199
	v_fmac_f32_e32 v99, v251, v251
	global_load_dwordx4 v[148:151], v[100:101], off offset:512
	global_load_dwordx4 v[152:155], v[102:103], off offset:1024
	global_load_dwordx4 v[156:159], v[102:103], off offset:1040
	global_load_dwordx4 v[160:163], v[100:101], off offset:544
	global_load_dwordx4 v[164:167], v[102:103], off offset:1088
	global_load_dwordx4 v[168:171], v[102:103], off offset:1104
	global_load_dwordx4 v[172:175], v[100:101], off offset:576
	global_load_dwordx4 v[176:179], v[102:103], off offset:1152
	global_load_dwordx4 v[180:183], v[102:103], off offset:1168
	global_load_dwordx4 v[184:187], v[100:101], off offset:608
	global_load_dwordx4 v[188:191], v[102:103], off offset:1216
	global_load_dwordx4 v[192:195], v[102:103], off offset:1232
	s_waitcnt vmcnt(42)
	v_mfma_f32_32x32x2_f32 v[0:15], v200, v140, v[0:15]
	v_lshlrev_b32_e32 v244, 16, v208
	v_fmac_f32_e32 v99, v140, v140
	v_mfma_f32_32x32x2_f32 v[0:15], v201, v141, v[0:15]
	v_and_b32_e32 v245, 0xffff0000, v208
	v_fmac_f32_e32 v99, v141, v141
	v_mfma_f32_32x32x2_f32 v[0:15], v202, v142, v[0:15]
	v_lshlrev_b32_e32 v246, 16, v209
	v_fmac_f32_e32 v99, v142, v142
	v_mfma_f32_32x32x2_f32 v[0:15], v203, v143, v[0:15]
	v_and_b32_e32 v247, 0xffff0000, v209
	v_fmac_f32_e32 v99, v143, v143
	v_mfma_f32_32x32x2_f32 v[0:15], v204, v144, v[0:15]
	v_lshlrev_b32_e32 v248, 16, v210
	v_fmac_f32_e32 v99, v144, v144
	v_mfma_f32_32x32x2_f32 v[0:15], v205, v145, v[0:15]
	v_and_b32_e32 v249, 0xffff0000, v210
	v_fmac_f32_e32 v99, v145, v145
	v_mfma_f32_32x32x2_f32 v[0:15], v206, v146, v[0:15]
	v_lshlrev_b32_e32 v250, 16, v211
	v_fmac_f32_e32 v99, v146, v146
	v_mfma_f32_32x32x2_f32 v[0:15], v207, v147, v[0:15]
	v_and_b32_e32 v251, 0xffff0000, v211
	v_fmac_f32_e32 v99, v147, v147
	s_waitcnt vmcnt(39)
	v_mfma_f32_32x32x2_f32 v[0:15], v212, v244, v[0:15]
	v_lshlrev_b32_e32 v140, 16, v220
	v_fmac_f32_e32 v99, v244, v244
	v_mfma_f32_32x32x2_f32 v[0:15], v213, v245, v[0:15]
	v_and_b32_e32 v141, 0xffff0000, v220
	v_fmac_f32_e32 v99, v245, v245
	v_mfma_f32_32x32x2_f32 v[0:15], v214, v246, v[0:15]
	v_lshlrev_b32_e32 v142, 16, v221
	v_fmac_f32_e32 v99, v246, v246
	v_mfma_f32_32x32x2_f32 v[0:15], v215, v247, v[0:15]
	v_and_b32_e32 v143, 0xffff0000, v221
	v_fmac_f32_e32 v99, v247, v247
	v_mfma_f32_32x32x2_f32 v[0:15], v216, v248, v[0:15]
	v_lshlrev_b32_e32 v144, 16, v222
	v_fmac_f32_e32 v99, v248, v248
	v_mfma_f32_32x32x2_f32 v[0:15], v217, v249, v[0:15]
	v_and_b32_e32 v145, 0xffff0000, v222
	v_fmac_f32_e32 v99, v249, v249
	v_mfma_f32_32x32x2_f32 v[0:15], v218, v250, v[0:15]
	v_lshlrev_b32_e32 v146, 16, v223
	v_fmac_f32_e32 v99, v250, v250
	v_mfma_f32_32x32x2_f32 v[0:15], v219, v251, v[0:15]
	v_and_b32_e32 v147, 0xffff0000, v223
	v_fmac_f32_e32 v99, v251, v251
	s_waitcnt vmcnt(36)
	v_mfma_f32_32x32x2_f32 v[0:15], v224, v140, v[0:15]
	v_lshlrev_b32_e32 v244, 16, v232
	v_fmac_f32_e32 v99, v140, v140
	v_mfma_f32_32x32x2_f32 v[0:15], v225, v141, v[0:15]
	v_and_b32_e32 v245, 0xffff0000, v232
	v_fmac_f32_e32 v99, v141, v141
	v_mfma_f32_32x32x2_f32 v[0:15], v226, v142, v[0:15]
	v_lshlrev_b32_e32 v246, 16, v233
	v_fmac_f32_e32 v99, v142, v142
	v_mfma_f32_32x32x2_f32 v[0:15], v227, v143, v[0:15]
	v_and_b32_e32 v247, 0xffff0000, v233
	v_fmac_f32_e32 v99, v143, v143
	v_mfma_f32_32x32x2_f32 v[0:15], v228, v144, v[0:15]
	v_lshlrev_b32_e32 v248, 16, v234
	v_fmac_f32_e32 v99, v144, v144
	v_mfma_f32_32x32x2_f32 v[0:15], v229, v145, v[0:15]
	v_and_b32_e32 v249, 0xffff0000, v234
	v_fmac_f32_e32 v99, v145, v145
	v_mfma_f32_32x32x2_f32 v[0:15], v230, v146, v[0:15]
	v_lshlrev_b32_e32 v250, 16, v235
	v_fmac_f32_e32 v99, v146, v146
	v_mfma_f32_32x32x2_f32 v[0:15], v231, v147, v[0:15]
	v_and_b32_e32 v251, 0xffff0000, v235
	v_fmac_f32_e32 v99, v147, v147
	s_waitcnt vmcnt(33)
; __device__ __forceinline__ float bf_lo(unsigned w) { return __uint_as_float(w << 16); }
; __device__ __forceinline__ float bf_hi(unsigned w) { return __uint_as_float(w & 0xffff0000u); }
; __global__ void __launch_bounds__(512, 2) fwd_kernel(Params p) {
;     ...
;                 u32x2 xb[2][8]; f32x4 wb[2][8];
; #pragma unroll
;                 for (int i = 0; i < 8; ++i) { xb[0][i] = *(const u32x2*)(xr + i * 8); wb[0][i] = *(const f32x4*)(wr_ + i * 8); }
; #pragma unroll
;                 for (int ch = 0; ch < 8; ++ch) {
;                     if (ch + 1 < 8) {
; #pragma unroll
;                         for (int i = 0; i < 8; ++i) { xb[(ch + 1) & 1][i] = *(const u32x2*)(xr + (ch + 1) * 64 + i * 8); wb[(ch + 1) & 1][i] = *(const f32x4*)(wr_ + (ch + 1) * 64 + i * 8); } }
; #pragma unroll
;                     for (int i = 0; i < 8; ++i) { const u32x2 xp = xb[ch & 1][i]; const f32x4 xv = {bf_lo(xp.x), bf_hi(xp.x), bf_lo(xp.y), bf_hi(xp.y)}, wv = wb[ch & 1][i];
;                         acc = __builtin_amdgcn_mfma_f32_32x32x2f32(wv.x, xv.x, acc, 0, 0, 0); acc = __builtin_amdgcn_mfma_f32_32x32x2f32(wv.y, xv.y, acc, 0, 0, 0);
;                         acc = __builtin_amdgcn_mfma_f32_32x32x2f32(wv.z, xv.z, acc, 0, 0, 0); acc = __builtin_amdgcn_mfma_f32_32x32x2f32(wv.w, xv.w, acc, 0, 0, 0);
;                         ss += (xv.x * xv.x + xv.y * xv.y) + (xv.z * xv.z + xv.w * xv.w); }
;                 }
	v_mfma_f32_32x32x2_f32 v[0:15], v236, v244, v[0:15]
	v_lshlrev_b32_e32 v140, 16, v16
	v_fmac_f32_e32 v99, v244, v244
	v_mfma_f32_32x32x2_f32 v[0:15], v237, v245, v[0:15]
	v_and_b32_e32 v141, 0xffff0000, v16
	v_fmac_f32_e32 v99, v245, v245
	v_mfma_f32_32x32x2_f32 v[0:15], v238, v246, v[0:15]
	v_lshlrev_b32_e32 v142, 16, v17
	v_fmac_f32_e32 v99, v246, v246
	v_mfma_f32_32x32x2_f32 v[0:15], v239, v247, v[0:15]
	v_and_b32_e32 v143, 0xffff0000, v17
	v_fmac_f32_e32 v99, v247, v247
	v_mfma_f32_32x32x2_f32 v[0:15], v240, v248, v[0:15]
	v_lshlrev_b32_e32 v144, 16, v18
	v_fmac_f32_e32 v99, v248, v248
	v_mfma_f32_32x32x2_f32 v[0:15], v241, v249, v[0:15]
	v_and_b32_e32 v145, 0xffff0000, v18
	v_fmac_f32_e32 v99, v249, v249
	v_mfma_f32_32x32x2_f32 v[0:15], v242, v250, v[0:15]
	v_lshlrev_b32_e32 v146, 16, v19
	v_fmac_f32_e32 v99, v250, v250
	v_mfma_f32_32x32x2_f32 v[0:15], v243, v251, v[0:15]
	v_and_b32_e32 v147, 0xffff0000, v19
	v_fmac_f32_e32 v99, v251, v251
	global_load_dwordx4 v[196:199], v[100:101], off offset:640
	global_load_dwordx4 v[200:203], v[102:103], off offset:1280
	global_load_dwordx4 v[204:207], v[102:103], off offset:1296
	global_load_dwordx4 v[208:211], v[100:101], off offset:672
	global_load_dwordx4 v[212:215], v[102:103], off offset:1344
	global_load_dwordx4 v[216:219], v[102:103], off offset:1360
	global_load_dwordx4 v[220:223], v[100:101], off offset:704
	global_load_dwordx4 v[224:227], v[102:103], off offset:1408
	global_load_dwordx4 v[228:231], v[102:103], off offset:1424
	global_load_dwordx4 v[232:235], v[100:101], off offset:736
	global_load_dwordx4 v[236:239], v[102:103], off offset:1472
	global_load_dwordx4 v[240:243], v[102:103], off offset:1488
	s_waitcnt vmcnt(42)
	v_mfma_f32_32x32x2_f32 v[0:15], v20, v140, v[0:15]
	v_lshlrev_b32_e32 v244, 16, v28
	v_fmac_f32_e32 v99, v140, v140
	v_mfma_f32_32x32x2_f32 v[0:15], v21, v141, v[0:15]
	v_and_b32_e32 v245, 0xffff0000, v28
	v_fmac_f32_e32 v99, v141, v141
	v_mfma_f32_32x32x2_f32 v[0:15], v22, v142, v[0:15]
	v_lshlrev_b32_e32 v246, 16, v29
	v_fmac_f32_e32 v99, v142, v142
	v_mfma_f32_32x32x2_f32 v[0:15], v23, v143, v[0:15]
	v_and_b32_e32 v247, 0xffff0000, v29
	v_fmac_f32_e32 v99, v143, v143
	v_mfma_f32_32x32x2_f32 v[0:15], v24, v144, v[0:15]
	v_lshlrev_b32_e32 v248, 16, v30
	v_fmac_f32_e32 v99, v144, v144
	v_mfma_f32_32x32x2_f32 v[0:15], v25, v145, v[0:15]
	v_and_b32_e32 v249, 0xffff0000, v30
	v_fmac_f32_e32 v99, v145, v145
	v_mfma_f32_32x32x2_f32 v[0:15], v26, v146, v[0:15]
	v_lshlrev_b32_e32 v250, 16, v31
	v_fmac_f32_e32 v99, v146, v146
	v_mfma_f32_32x32x2_f32 v[0:15], v27, v147, v[0:15]
	v_and_b32_e32 v251, 0xffff0000, v31
	v_fmac_f32_e32 v99, v147, v147
	s_waitcnt vmcnt(39)
	v_mfma_f32_32x32x2_f32 v[0:15], v32, v244, v[0:15]
	v_lshlrev_b32_e32 v140, 16, v40
	v_fmac_f32_e32 v99, v244, v244
	v_mfma_f32_32x32x2_f32 v[0:15], v33, v245, v[0:15]
	v_and_b32_e32 v141, 0xffff0000, v40
	v_fmac_f32_e32 v99, v245, v245
	v_mfma_f32_32x32x2_f32 v[0:15], v34, v246, v[0:15]
	v_lshlrev_b32_e32 v142, 16, v41
	v_fmac_f32_e32 v99, v246, v246
	v_mfma_f32_32x32x2_f32 v[0:15], v35, v247, v[0:15]
	v_and_b32_e32 v143, 0xffff0000, v41
	v_fmac_f32_e32 v99, v247, v247
	v_mfma_f32_32x32x2_f32 v[0:15], v36, v248, v[0:15]
	v_lshlrev_b32_e32 v144, 16, v42
	v_fmac_f32_e32 v99, v248, v248
	v_mfma_f32_32x32x2_f32 v[0:15], v37, v249, v[0:15]
	v_and_b32_e32 v145, 0xffff0000, v42
	v_fmac_f32_e32 v99, v249, v249
	v_mfma_f32_32x32x2_f32 v[0:15], v38, v250, v[0:15]
	v_lshlrev_b32_e32 v146, 16, v43
	v_fmac_f32_e32 v99, v250, v250
	v_mfma_f32_32x32x2_f32 v[0:15], v39, v251, v[0:15]
	v_and_b32_e32 v147, 0xffff0000, v43
	v_fmac_f32_e32 v99, v251, v251
	s_waitcnt vmcnt(36)
	v_mfma_f32_32x32x2_f32 v[0:15], v44, v140, v[0:15]
	v_lshlrev_b32_e32 v244, 16, v52
	v_fmac_f32_e32 v99, v140, v140
	v_mfma_f32_32x32x2_f32 v[0:15], v45, v141, v[0:15]
	v_and_b32_e32 v245, 0xffff0000, v52
	v_fmac_f32_e32 v99, v141, v141
	v_mfma_f32_32x32x2_f32 v[0:15], v46, v142, v[0:15]
	v_lshlrev_b32_e32 v246, 16, v53
	v_fmac_f32_e32 v99, v142, v142
	v_mfma_f32_32x32x2_f32 v[0:15], v47, v143, v[0:15]
	v_and_b32_e32 v247, 0xffff0000, v53
	v_fmac_f32_e32 v99, v143, v143
	v_mfma_f32_32x32x2_f32 v[0:15], v48, v144, v[0:15]
	v_lshlrev_b32_e32 v248, 16, v54
	v_fmac_f32_e32 v99, v144, v144
	v_mfma_f32_32x32x2_f32 v[0:15], v49, v145, v[0:15]
	v_and_b32_e32 v249, 0xffff0000, v54
	v_fmac_f32_e32 v99, v145, v145
	v_mfma_f32_32x32x2_f32 v[0:15], v50, v146, v[0:15]
	v_lshlrev_b32_e32 v250, 16, v55
	v_fmac_f32_e32 v99, v146, v146
	v_mfma_f32_32x32x2_f32 v[0:15], v51, v147, v[0:15]
	v_and_b32_e32 v251, 0xffff0000, v55
	v_fmac_f32_e32 v99, v147, v147
	s_waitcnt vmcnt(33)
	v_mfma_f32_32x32x2_f32 v[0:15], v56, v244, v[0:15]
	v_lshlrev_b32_e32 v140, 16, v64
	v_fmac_f32_e32 v99, v244, v244
	v_mfma_f32_32x32x2_f32 v[0:15], v57, v245, v[0:15]
	v_and_b32_e32 v141, 0xffff0000, v64
	v_fmac_f32_e32 v99, v245, v245
	v_mfma_f32_32x32x2_f32 v[0:15], v58, v246, v[0:15]
	v_lshlrev_b32_e32 v142, 16, v65
	v_fmac_f32_e32 v99, v246, v246
	v_mfma_f32_32x32x2_f32 v[0:15], v59, v247, v[0:15]
	v_and_b32_e32 v143, 0xffff0000, v65
	v_fmac_f32_e32 v99, v247, v247
	v_mfma_f32_32x32x2_f32 v[0:15], v60, v248, v[0:15]
	v_lshlrev_b32_e32 v144, 16, v66
	v_fmac_f32_e32 v99, v248, v248
	v_mfma_f32_32x32x2_f32 v[0:15], v61, v249, v[0:15]
	v_and_b32_e32 v145, 0xffff0000, v66
	v_fmac_f32_e32 v99, v249, v249
	v_mfma_f32_32x32x2_f32 v[0:15], v62, v250, v[0:15]
	v_lshlrev_b32_e32 v146, 16, v67
	v_fmac_f32_e32 v99, v250, v250
	v_mfma_f32_32x32x2_f32 v[0:15], v63, v251, v[0:15]
	v_and_b32_e32 v147, 0xffff0000, v67
	v_fmac_f32_e32 v99, v251, v251
	global_load_dwordx4 v[16:19], v[100:101], off offset:768
	global_load_dwordx4 v[20:23], v[102:103], off offset:1536
	global_load_dwordx4 v[24:27], v[102:103], off offset:1552
	global_load_dwordx4 v[28:31], v[100:101], off offset:800
	global_load_dwordx4 v[32:35], v[102:103], off offset:1600
	global_load_dwordx4 v[36:39], v[102:103], off offset:1616
	global_load_dwordx4 v[40:43], v[100:101], off offset:832
	global_load_dwordx4 v[44:47], v[102:103], off offset:1664
	global_load_dwordx4 v[48:51], v[102:103], off offset:1680
	global_load_dwordx4 v[52:55], v[100:101], off offset:864
	global_load_dwordx4 v[56:59], v[102:103], off offset:1728
	global_load_dwordx4 v[60:63], v[102:103], off offset:1744
	s_waitcnt vmcnt(42)
; __device__ __forceinline__ float bf_lo(unsigned w) { return __uint_as_float(w << 16); }
; __device__ __forceinline__ float bf_hi(unsigned w) { return __uint_as_float(w & 0xffff0000u); }
; __global__ void __launch_bounds__(512, 2) fwd_kernel(Params p) {
;     ...
;                 u32x2 xb[2][8]; f32x4 wb[2][8];
; #pragma unroll
;                 for (int i = 0; i < 8; ++i) { xb[0][i] = *(const u32x2*)(xr + i * 8); wb[0][i] = *(const f32x4*)(wr_ + i * 8); }
; #pragma unroll
;                 for (int ch = 0; ch < 8; ++ch) {
;                     if (ch + 1 < 8) {
; #pragma unroll
;                         for (int i = 0; i < 8; ++i) { xb[(ch + 1) & 1][i] = *(const u32x2*)(xr + (ch + 1) * 64 + i * 8); wb[(ch + 1) & 1][i] = *(const f32x4*)(wr_ + (ch + 1) * 64 + i * 8); } }
; #pragma unroll
;                     for (int i = 0; i < 8; ++i) { const u32x2 xp = xb[ch & 1][i]; const f32x4 xv = {bf_lo(xp.x), bf_hi(xp.x), bf_lo(xp.y), bf_hi(xp.y)}, wv = wb[ch & 1][i];
;                         acc = __builtin_amdgcn_mfma_f32_32x32x2f32(wv.x, xv.x, acc, 0, 0, 0); acc = __builtin_amdgcn_mfma_f32_32x32x2f32(wv.y, xv.y, acc, 0, 0, 0);
;                         acc = __builtin_amdgcn_mfma_f32_32x32x2f32(wv.z, xv.z, acc, 0, 0, 0); acc = __builtin_amdgcn_mfma_f32_32x32x2f32(wv.w, xv.w, acc, 0, 0, 0);
;                         ss += (xv.x * xv.x + xv.y * xv.y) + (xv.z * xv.z + xv.w * xv.w); }
;                 }
	v_mfma_f32_32x32x2_f32 v[0:15], v68, v140, v[0:15]
	v_lshlrev_b32_e32 v244, 16, v76
	v_fmac_f32_e32 v99, v140, v140
	v_mfma_f32_32x32x2_f32 v[0:15], v69, v141, v[0:15]
	v_and_b32_e32 v245, 0xffff0000, v76
	v_fmac_f32_e32 v99, v141, v141
	v_mfma_f32_32x32x2_f32 v[0:15], v70, v142, v[0:15]
	v_lshlrev_b32_e32 v246, 16, v77
	v_fmac_f32_e32 v99, v142, v142
	v_mfma_f32_32x32x2_f32 v[0:15], v71, v143, v[0:15]
	v_and_b32_e32 v247, 0xffff0000, v77
	v_fmac_f32_e32 v99, v143, v143
	v_mfma_f32_32x32x2_f32 v[0:15], v72, v144, v[0:15]
	v_lshlrev_b32_e32 v248, 16, v78
	v_fmac_f32_e32 v99, v144, v144
	v_mfma_f32_32x32x2_f32 v[0:15], v73, v145, v[0:15]
	v_and_b32_e32 v249, 0xffff0000, v78
	v_fmac_f32_e32 v99, v145, v145
	v_mfma_f32_32x32x2_f32 v[0:15], v74, v146, v[0:15]
	v_lshlrev_b32_e32 v250, 16, v79
	v_fmac_f32_e32 v99, v146, v146
	v_mfma_f32_32x32x2_f32 v[0:15], v75, v147, v[0:15]
	v_and_b32_e32 v251, 0xffff0000, v79
	v_fmac_f32_e32 v99, v147, v147
	s_waitcnt vmcnt(39)
	v_mfma_f32_32x32x2_f32 v[0:15], v80, v244, v[0:15]
	v_lshlrev_b32_e32 v140, 16, v108
	v_fmac_f32_e32 v99, v244, v244
	v_mfma_f32_32x32x2_f32 v[0:15], v81, v245, v[0:15]
	v_and_b32_e32 v141, 0xffff0000, v108
	v_fmac_f32_e32 v99, v245, v245
	v_mfma_f32_32x32x2_f32 v[0:15], v82, v246, v[0:15]
	v_lshlrev_b32_e32 v142, 16, v109
	v_fmac_f32_e32 v99, v246, v246
	v_mfma_f32_32x32x2_f32 v[0:15], v83, v247, v[0:15]
	v_and_b32_e32 v143, 0xffff0000, v109
	v_fmac_f32_e32 v99, v247, v247
	v_mfma_f32_32x32x2_f32 v[0:15], v104, v248, v[0:15]
	v_lshlrev_b32_e32 v144, 16, v110
	v_fmac_f32_e32 v99, v248, v248
	v_mfma_f32_32x32x2_f32 v[0:15], v105, v249, v[0:15]
	v_and_b32_e32 v145, 0xffff0000, v110
	v_fmac_f32_e32 v99, v249, v249
	v_mfma_f32_32x32x2_f32 v[0:15], v106, v250, v[0:15]
	v_lshlrev_b32_e32 v146, 16, v111
	v_fmac_f32_e32 v99, v250, v250
	v_mfma_f32_32x32x2_f32 v[0:15], v107, v251, v[0:15]
	v_and_b32_e32 v147, 0xffff0000, v111
	v_fmac_f32_e32 v99, v251, v251
	s_waitcnt vmcnt(36)
	v_mfma_f32_32x32x2_f32 v[0:15], v112, v140, v[0:15]
	v_lshlrev_b32_e32 v244, 16, v120
	v_fmac_f32_e32 v99, v140, v140
	v_mfma_f32_32x32x2_f32 v[0:15], v113, v141, v[0:15]
	v_and_b32_e32 v245, 0xffff0000, v120
	v_fmac_f32_e32 v99, v141, v141
	v_mfma_f32_32x32x2_f32 v[0:15], v114, v142, v[0:15]
	v_lshlrev_b32_e32 v246, 16, v121
	v_fmac_f32_e32 v99, v142, v142
	v_mfma_f32_32x32x2_f32 v[0:15], v115, v143, v[0:15]
	v_and_b32_e32 v247, 0xffff0000, v121
	v_fmac_f32_e32 v99, v143, v143
	v_mfma_f32_32x32x2_f32 v[0:15], v116, v144, v[0:15]
	v_lshlrev_b32_e32 v248, 16, v122
	v_fmac_f32_e32 v99, v144, v144
	v_mfma_f32_32x32x2_f32 v[0:15], v117, v145, v[0:15]
	v_and_b32_e32 v249, 0xffff0000, v122
	v_fmac_f32_e32 v99, v145, v145
	v_mfma_f32_32x32x2_f32 v[0:15], v118, v146, v[0:15]
	v_lshlrev_b32_e32 v250, 16, v123
	v_fmac_f32_e32 v99, v146, v146
	v_mfma_f32_32x32x2_f32 v[0:15], v119, v147, v[0:15]
	v_and_b32_e32 v251, 0xffff0000, v123
	v_fmac_f32_e32 v99, v147, v147
	s_waitcnt vmcnt(33)
	v_mfma_f32_32x32x2_f32 v[0:15], v124, v244, v[0:15]
	v_lshlrev_b32_e32 v140, 16, v148
	v_fmac_f32_e32 v99, v244, v244
	v_mfma_f32_32x32x2_f32 v[0:15], v125, v245, v[0:15]
	v_and_b32_e32 v141, 0xffff0000, v148
	v_fmac_f32_e32 v99, v245, v245
	v_mfma_f32_32x32x2_f32 v[0:15], v126, v246, v[0:15]
	v_lshlrev_b32_e32 v142, 16, v149
	v_fmac_f32_e32 v99, v246, v246
	v_mfma_f32_32x32x2_f32 v[0:15], v127, v247, v[0:15]
	v_and_b32_e32 v143, 0xffff0000, v149
	v_fmac_f32_e32 v99, v247, v247
	v_mfma_f32_32x32x2_f32 v[0:15], v128, v248, v[0:15]
	v_lshlrev_b32_e32 v144, 16, v150
	v_fmac_f32_e32 v99, v248, v248
	v_mfma_f32_32x32x2_f32 v[0:15], v129, v249, v[0:15]
	v_and_b32_e32 v145, 0xffff0000, v150
	v_fmac_f32_e32 v99, v249, v249
	v_mfma_f32_32x32x2_f32 v[0:15], v130, v250, v[0:15]
	v_lshlrev_b32_e32 v146, 16, v151
	v_fmac_f32_e32 v99, v250, v250
	v_mfma_f32_32x32x2_f32 v[0:15], v131, v251, v[0:15]
	v_and_b32_e32 v147, 0xffff0000, v151
	v_fmac_f32_e32 v99, v251, v251
	global_load_dwordx4 v[64:67], v[100:101], off offset:896
	global_load_dwordx4 v[68:71], v[102:103], off offset:1792
	global_load_dwordx4 v[72:75], v[102:103], off offset:1808
	global_load_dwordx4 v[76:79], v[100:101], off offset:928
	global_load_dwordx4 v[80:83], v[102:103], off offset:1856
	global_load_dwordx4 v[104:107], v[102:103], off offset:1872
	global_load_dwordx4 v[108:111], v[100:101], off offset:960
	global_load_dwordx4 v[112:115], v[102:103], off offset:1920
	global_load_dwordx4 v[116:119], v[102:103], off offset:1936
	global_load_dwordx4 v[120:123], v[100:101], off offset:992
	global_load_dwordx4 v[124:127], v[102:103], off offset:1984
	global_load_dwordx4 v[128:131], v[102:103], off offset:2000
	s_waitcnt vmcnt(42)
	v_mfma_f32_32x32x2_f32 v[0:15], v152, v140, v[0:15]
	v_lshlrev_b32_e32 v244, 16, v160
	v_fmac_f32_e32 v99, v140, v140
	v_mfma_f32_32x32x2_f32 v[0:15], v153, v141, v[0:15]
	v_and_b32_e32 v245, 0xffff0000, v160
	v_fmac_f32_e32 v99, v141, v141
	v_mfma_f32_32x32x2_f32 v[0:15], v154, v142, v[0:15]
	v_lshlrev_b32_e32 v246, 16, v161
	v_fmac_f32_e32 v99, v142, v142
	v_mfma_f32_32x32x2_f32 v[0:15], v155, v143, v[0:15]
	v_and_b32_e32 v247, 0xffff0000, v161
	v_fmac_f32_e32 v99, v143, v143
	v_mfma_f32_32x32x2_f32 v[0:15], v156, v144, v[0:15]
	v_lshlrev_b32_e32 v248, 16, v162
	v_fmac_f32_e32 v99, v144, v144
	v_mfma_f32_32x32x2_f32 v[0:15], v157, v145, v[0:15]
	v_and_b32_e32 v249, 0xffff0000, v162
	v_fmac_f32_e32 v99, v145, v145
	v_mfma_f32_32x32x2_f32 v[0:15], v158, v146, v[0:15]
	v_lshlrev_b32_e32 v250, 16, v163
	v_fmac_f32_e32 v99, v146, v146
	v_mfma_f32_32x32x2_f32 v[0:15], v159, v147, v[0:15]
	v_and_b32_e32 v251, 0xffff0000, v163
	v_fmac_f32_e32 v99, v147, v147
	s_waitcnt vmcnt(39)
; __device__ __forceinline__ float bf_lo(unsigned w) { return __uint_as_float(w << 16); }
; __device__ __forceinline__ float bf_hi(unsigned w) { return __uint_as_float(w & 0xffff0000u); }
; __global__ void __launch_bounds__(512, 2) fwd_kernel(Params p) {
;     ...
;                 u32x2 xb[2][8]; f32x4 wb[2][8];
; #pragma unroll
;                 for (int i = 0; i < 8; ++i) { xb[0][i] = *(const u32x2*)(xr + i * 8); wb[0][i] = *(const f32x4*)(wr_ + i * 8); }
; #pragma unroll
;                 for (int ch = 0; ch < 8; ++ch) {
;                     if (ch + 1 < 8) {
; #pragma unroll
;                         for (int i = 0; i < 8; ++i) { xb[(ch + 1) & 1][i] = *(const u32x2*)(xr + (ch + 1) * 64 + i * 8); wb[(ch + 1) & 1][i] = *(const f32x4*)(wr_ + (ch + 1) * 64 + i * 8); } }
; #pragma unroll
;                     for (int i = 0; i < 8; ++i) { const u32x2 xp = xb[ch & 1][i]; const f32x4 xv = {bf_lo(xp.x), bf_hi(xp.x), bf_lo(xp.y), bf_hi(xp.y)}, wv = wb[ch & 1][i];
;                         acc = __builtin_amdgcn_mfma_f32_32x32x2f32(wv.x, xv.x, acc, 0, 0, 0); acc = __builtin_amdgcn_mfma_f32_32x32x2f32(wv.y, xv.y, acc, 0, 0, 0);
;                         acc = __builtin_amdgcn_mfma_f32_32x32x2f32(wv.z, xv.z, acc, 0, 0, 0); acc = __builtin_amdgcn_mfma_f32_32x32x2f32(wv.w, xv.w, acc, 0, 0, 0);
;                         ss += (xv.x * xv.x + xv.y * xv.y) + (xv.z * xv.z + xv.w * xv.w); }
;                 }
	v_mfma_f32_32x32x2_f32 v[0:15], v164, v244, v[0:15]
	v_lshlrev_b32_e32 v140, 16, v172
	v_fmac_f32_e32 v99, v244, v244
	v_mfma_f32_32x32x2_f32 v[0:15], v165, v245, v[0:15]
	v_and_b32_e32 v141, 0xffff0000, v172
	v_fmac_f32_e32 v99, v245, v245
	v_mfma_f32_32x32x2_f32 v[0:15], v166, v246, v[0:15]
	v_lshlrev_b32_e32 v142, 16, v173
	v_fmac_f32_e32 v99, v246, v246
	v_mfma_f32_32x32x2_f32 v[0:15], v167, v247, v[0:15]
	v_and_b32_e32 v143, 0xffff0000, v173
	v_fmac_f32_e32 v99, v247, v247
	v_mfma_f32_32x32x2_f32 v[0:15], v168, v248, v[0:15]
	v_lshlrev_b32_e32 v144, 16, v174
	v_fmac_f32_e32 v99, v248, v248
	v_mfma_f32_32x32x2_f32 v[0:15], v169, v249, v[0:15]
	v_and_b32_e32 v145, 0xffff0000, v174
	v_fmac_f32_e32 v99, v249, v249
	v_mfma_f32_32x32x2_f32 v[0:15], v170, v250, v[0:15]
	v_lshlrev_b32_e32 v146, 16, v175
	v_fmac_f32_e32 v99, v250, v250
	v_mfma_f32_32x32x2_f32 v[0:15], v171, v251, v[0:15]
	v_and_b32_e32 v147, 0xffff0000, v175
	v_fmac_f32_e32 v99, v251, v251
	s_waitcnt vmcnt(36)
	v_mfma_f32_32x32x2_f32 v[0:15], v176, v140, v[0:15]
	v_lshlrev_b32_e32 v244, 16, v184
	v_fmac_f32_e32 v99, v140, v140
	v_mfma_f32_32x32x2_f32 v[0:15], v177, v141, v[0:15]
	v_and_b32_e32 v245, 0xffff0000, v184
	v_fmac_f32_e32 v99, v141, v141
	v_mfma_f32_32x32x2_f32 v[0:15], v178, v142, v[0:15]
	v_lshlrev_b32_e32 v246, 16, v185
	v_fmac_f32_e32 v99, v142, v142
	v_mfma_f32_32x32x2_f32 v[0:15], v179, v143, v[0:15]
	v_and_b32_e32 v247, 0xffff0000, v185
	v_fmac_f32_e32 v99, v143, v143
	v_mfma_f32_32x32x2_f32 v[0:15], v180, v144, v[0:15]
	v_lshlrev_b32_e32 v248, 16, v186
	v_fmac_f32_e32 v99, v144, v144
	v_mfma_f32_32x32x2_f32 v[0:15], v181, v145, v[0:15]
	v_and_b32_e32 v249, 0xffff0000, v186
	v_fmac_f32_e32 v99, v145, v145
	v_mfma_f32_32x32x2_f32 v[0:15], v182, v146, v[0:15]
	v_lshlrev_b32_e32 v250, 16, v187
	v_fmac_f32_e32 v99, v146, v146
	v_mfma_f32_32x32x2_f32 v[0:15], v183, v147, v[0:15]
	v_and_b32_e32 v251, 0xffff0000, v187
	v_fmac_f32_e32 v99, v147, v147
	s_waitcnt vmcnt(33)
	v_mfma_f32_32x32x2_f32 v[0:15], v188, v244, v[0:15]
	v_lshlrev_b32_e32 v140, 16, v196
	v_fmac_f32_e32 v99, v244, v244
	v_mfma_f32_32x32x2_f32 v[0:15], v189, v245, v[0:15]
	v_and_b32_e32 v141, 0xffff0000, v196
	v_fmac_f32_e32 v99, v245, v245
	v_mfma_f32_32x32x2_f32 v[0:15], v190, v246, v[0:15]
	v_lshlrev_b32_e32 v142, 16, v197
	v_fmac_f32_e32 v99, v246, v246
	v_mfma_f32_32x32x2_f32 v[0:15], v191, v247, v[0:15]
	v_and_b32_e32 v143, 0xffff0000, v197
	v_fmac_f32_e32 v99, v247, v247
	v_mfma_f32_32x32x2_f32 v[0:15], v192, v248, v[0:15]
	v_lshlrev_b32_e32 v144, 16, v198
	v_fmac_f32_e32 v99, v248, v248
	v_mfma_f32_32x32x2_f32 v[0:15], v193, v249, v[0:15]
	v_and_b32_e32 v145, 0xffff0000, v198
	v_fmac_f32_e32 v99, v249, v249
	v_mfma_f32_32x32x2_f32 v[0:15], v194, v250, v[0:15]
	v_lshlrev_b32_e32 v146, 16, v199
	v_fmac_f32_e32 v99, v250, v250
	v_mfma_f32_32x32x2_f32 v[0:15], v195, v251, v[0:15]
	v_and_b32_e32 v147, 0xffff0000, v199
	v_fmac_f32_e32 v99, v251, v251
	s_waitcnt vmcnt(30)
	v_mfma_f32_32x32x2_f32 v[0:15], v200, v140, v[0:15]
	v_lshlrev_b32_e32 v244, 16, v208
	v_fmac_f32_e32 v99, v140, v140
	v_mfma_f32_32x32x2_f32 v[0:15], v201, v141, v[0:15]
	v_and_b32_e32 v245, 0xffff0000, v208
	v_fmac_f32_e32 v99, v141, v141
	v_mfma_f32_32x32x2_f32 v[0:15], v202, v142, v[0:15]
	v_lshlrev_b32_e32 v246, 16, v209
	v_fmac_f32_e32 v99, v142, v142
	v_mfma_f32_32x32x2_f32 v[0:15], v203, v143, v[0:15]
	v_and_b32_e32 v247, 0xffff0000, v209
	v_fmac_f32_e32 v99, v143, v143
	v_mfma_f32_32x32x2_f32 v[0:15], v204, v144, v[0:15]
	v_lshlrev_b32_e32 v248, 16, v210
	v_fmac_f32_e32 v99, v144, v144
	v_mfma_f32_32x32x2_f32 v[0:15], v205, v145, v[0:15]
	v_and_b32_e32 v249, 0xffff0000, v210
	v_fmac_f32_e32 v99, v145, v145
	v_mfma_f32_32x32x2_f32 v[0:15], v206, v146, v[0:15]
	v_lshlrev_b32_e32 v250, 16, v211
	v_fmac_f32_e32 v99, v146, v146
	v_mfma_f32_32x32x2_f32 v[0:15], v207, v147, v[0:15]
	v_and_b32_e32 v251, 0xffff0000, v211
	v_fmac_f32_e32 v99, v147, v147
	s_waitcnt vmcnt(27)
	v_mfma_f32_32x32x2_f32 v[0:15], v212, v244, v[0:15]
	v_lshlrev_b32_e32 v140, 16, v220
	v_fmac_f32_e32 v99, v244, v244
	v_mfma_f32_32x32x2_f32 v[0:15], v213, v245, v[0:15]
	v_and_b32_e32 v141, 0xffff0000, v220
	v_fmac_f32_e32 v99, v245, v245
	v_mfma_f32_32x32x2_f32 v[0:15], v214, v246, v[0:15]
	v_lshlrev_b32_e32 v142, 16, v221
	v_fmac_f32_e32 v99, v246, v246
	v_mfma_f32_32x32x2_f32 v[0:15], v215, v247, v[0:15]
	v_and_b32_e32 v143, 0xffff0000, v221
	v_fmac_f32_e32 v99, v247, v247
	v_mfma_f32_32x32x2_f32 v[0:15], v216, v248, v[0:15]
	v_lshlrev_b32_e32 v144, 16, v222
	v_fmac_f32_e32 v99, v248, v248
	v_mfma_f32_32x32x2_f32 v[0:15], v217, v249, v[0:15]
	v_and_b32_e32 v145, 0xffff0000, v222
	v_fmac_f32_e32 v99, v249, v249
	v_mfma_f32_32x32x2_f32 v[0:15], v218, v250, v[0:15]
	v_lshlrev_b32_e32 v146, 16, v223
	v_fmac_f32_e32 v99, v250, v250
	v_mfma_f32_32x32x2_f32 v[0:15], v219, v251, v[0:15]
	v_and_b32_e32 v147, 0xffff0000, v223
	v_fmac_f32_e32 v99, v251, v251
	s_waitcnt vmcnt(24)
	v_mfma_f32_32x32x2_f32 v[0:15], v224, v140, v[0:15]
	v_lshlrev_b32_e32 v244, 16, v232
	v_fmac_f32_e32 v99, v140, v140
	v_mfma_f32_32x32x2_f32 v[0:15], v225, v141, v[0:15]
	v_and_b32_e32 v245, 0xffff0000, v232
	v_fmac_f32_e32 v99, v141, v141
	v_mfma_f32_32x32x2_f32 v[0:15], v226, v142, v[0:15]
	v_lshlrev_b32_e32 v246, 16, v233
	v_fmac_f32_e32 v99, v142, v142
	v_mfma_f32_32x32x2_f32 v[0:15], v227, v143, v[0:15]
	v_and_b32_e32 v247, 0xffff0000, v233
	v_fmac_f32_e32 v99, v143, v143
	v_mfma_f32_32x32x2_f32 v[0:15], v228, v144, v[0:15]
	v_lshlrev_b32_e32 v248, 16, v234
	v_fmac_f32_e32 v99, v144, v144
	v_mfma_f32_32x32x2_f32 v[0:15], v229, v145, v[0:15]
	v_and_b32_e32 v249, 0xffff0000, v234
	v_fmac_f32_e32 v99, v145, v145
	v_mfma_f32_32x32x2_f32 v[0:15], v230, v146, v[0:15]
	v_lshlrev_b32_e32 v250, 16, v235
	v_fmac_f32_e32 v99, v146, v146
	v_mfma_f32_32x32x2_f32 v[0:15], v231, v147, v[0:15]
	v_and_b32_e32 v251, 0xffff0000, v235
	v_fmac_f32_e32 v99, v147, v147
	s_waitcnt vmcnt(21)
; __device__ __forceinline__ float bf_lo(unsigned w) { return __uint_as_float(w << 16); }
; __device__ __forceinline__ float bf_hi(unsigned w) { return __uint_as_float(w & 0xffff0000u); }
; __global__ void __launch_bounds__(512, 2) fwd_kernel(Params p) {
;     ...
;                 u32x2 xb[2][8]; f32x4 wb[2][8];
; #pragma unroll
;                 for (int i = 0; i < 8; ++i) { xb[0][i] = *(const u32x2*)(xr + i * 8); wb[0][i] = *(const f32x4*)(wr_ + i * 8); }
; #pragma unroll
;                 for (int ch = 0; ch < 8; ++ch) {
;                     if (ch + 1 < 8) {
; #pragma unroll
;                         for (int i = 0; i < 8; ++i) { xb[(ch + 1) & 1][i] = *(const u32x2*)(xr + (ch + 1) * 64 + i * 8); wb[(ch + 1) & 1][i] = *(const f32x4*)(wr_ + (ch + 1) * 64 + i * 8); } }
; #pragma unroll
;                     for (int i = 0; i < 8; ++i) { const u32x2 xp = xb[ch & 1][i]; const f32x4 xv = {bf_lo(xp.x), bf_hi(xp.x), bf_lo(xp.y), bf_hi(xp.y)}, wv = wb[ch & 1][i];
;                         acc = __builtin_amdgcn_mfma_f32_32x32x2f32(wv.x, xv.x, acc, 0, 0, 0); acc = __builtin_amdgcn_mfma_f32_32x32x2f32(wv.y, xv.y, acc, 0, 0, 0);
;                         acc = __builtin_amdgcn_mfma_f32_32x32x2f32(wv.z, xv.z, acc, 0, 0, 0); acc = __builtin_amdgcn_mfma_f32_32x32x2f32(wv.w, xv.w, acc, 0, 0, 0);
;                         ss += (xv.x * xv.x + xv.y * xv.y) + (xv.z * xv.z + xv.w * xv.w); }
;                 }
	v_mfma_f32_32x32x2_f32 v[0:15], v236, v244, v[0:15]
	v_lshlrev_b32_e32 v140, 16, v16
	v_fmac_f32_e32 v99, v244, v244
	v_mfma_f32_32x32x2_f32 v[0:15], v237, v245, v[0:15]
	v_and_b32_e32 v141, 0xffff0000, v16
	v_fmac_f32_e32 v99, v245, v245
	v_mfma_f32_32x32x2_f32 v[0:15], v238, v246, v[0:15]
	v_lshlrev_b32_e32 v142, 16, v17
	v_fmac_f32_e32 v99, v246, v246
	v_mfma_f32_32x32x2_f32 v[0:15], v239, v247, v[0:15]
	v_and_b32_e32 v143, 0xffff0000, v17
	v_fmac_f32_e32 v99, v247, v247
	v_mfma_f32_32x32x2_f32 v[0:15], v240, v248, v[0:15]
	v_lshlrev_b32_e32 v144, 16, v18
	v_fmac_f32_e32 v99, v248, v248
	v_mfma_f32_32x32x2_f32 v[0:15], v241, v249, v[0:15]
	v_and_b32_e32 v145, 0xffff0000, v18
	v_fmac_f32_e32 v99, v249, v249
	v_mfma_f32_32x32x2_f32 v[0:15], v242, v250, v[0:15]
	v_lshlrev_b32_e32 v146, 16, v19
	v_fmac_f32_e32 v99, v250, v250
	v_mfma_f32_32x32x2_f32 v[0:15], v243, v251, v[0:15]
	v_and_b32_e32 v147, 0xffff0000, v19
	v_fmac_f32_e32 v99, v251, v251
	s_waitcnt vmcnt(18)
	v_mfma_f32_32x32x2_f32 v[0:15], v20, v140, v[0:15]
	v_lshlrev_b32_e32 v244, 16, v28
	v_fmac_f32_e32 v99, v140, v140
	v_mfma_f32_32x32x2_f32 v[0:15], v21, v141, v[0:15]
	v_and_b32_e32 v245, 0xffff0000, v28
	v_fmac_f32_e32 v99, v141, v141
	v_mfma_f32_32x32x2_f32 v[0:15], v22, v142, v[0:15]
	v_lshlrev_b32_e32 v246, 16, v29
	v_fmac_f32_e32 v99, v142, v142
	v_mfma_f32_32x32x2_f32 v[0:15], v23, v143, v[0:15]
	v_and_b32_e32 v247, 0xffff0000, v29
	v_fmac_f32_e32 v99, v143, v143
	v_mfma_f32_32x32x2_f32 v[0:15], v24, v144, v[0:15]
	v_lshlrev_b32_e32 v248, 16, v30
	v_fmac_f32_e32 v99, v144, v144
	v_mfma_f32_32x32x2_f32 v[0:15], v25, v145, v[0:15]
	v_and_b32_e32 v249, 0xffff0000, v30
	v_fmac_f32_e32 v99, v145, v145
	v_mfma_f32_32x32x2_f32 v[0:15], v26, v146, v[0:15]
	v_lshlrev_b32_e32 v250, 16, v31
	v_fmac_f32_e32 v99, v146, v146
	v_mfma_f32_32x32x2_f32 v[0:15], v27, v147, v[0:15]
	v_and_b32_e32 v251, 0xffff0000, v31
	v_fmac_f32_e32 v99, v147, v147
	s_waitcnt vmcnt(15)
	v_mfma_f32_32x32x2_f32 v[0:15], v32, v244, v[0:15]
	v_lshlrev_b32_e32 v140, 16, v40
	v_fmac_f32_e32 v99, v244, v244
	v_mfma_f32_32x32x2_f32 v[0:15], v33, v245, v[0:15]
	v_and_b32_e32 v141, 0xffff0000, v40
	v_fmac_f32_e32 v99, v245, v245
	v_mfma_f32_32x32x2_f32 v[0:15], v34, v246, v[0:15]
	v_lshlrev_b32_e32 v142, 16, v41
	v_fmac_f32_e32 v99, v246, v246
	v_mfma_f32_32x32x2_f32 v[0:15], v35, v247, v[0:15]
	v_and_b32_e32 v143, 0xffff0000, v41
	v_fmac_f32_e32 v99, v247, v247
	v_mfma_f32_32x32x2_f32 v[0:15], v36, v248, v[0:15]
	v_lshlrev_b32_e32 v144, 16, v42
	v_fmac_f32_e32 v99, v248, v248
	v_mfma_f32_32x32x2_f32 v[0:15], v37, v249, v[0:15]
	v_and_b32_e32 v145, 0xffff0000, v42
	v_fmac_f32_e32 v99, v249, v249
	v_mfma_f32_32x32x2_f32 v[0:15], v38, v250, v[0:15]
	v_lshlrev_b32_e32 v146, 16, v43
	v_fmac_f32_e32 v99, v250, v250
	v_mfma_f32_32x32x2_f32 v[0:15], v39, v251, v[0:15]
	v_and_b32_e32 v147, 0xffff0000, v43
	v_fmac_f32_e32 v99, v251, v251
	s_waitcnt vmcnt(12)
	v_mfma_f32_32x32x2_f32 v[0:15], v44, v140, v[0:15]
	v_lshlrev_b32_e32 v244, 16, v52
	v_fmac_f32_e32 v99, v140, v140
	v_mfma_f32_32x32x2_f32 v[0:15], v45, v141, v[0:15]
	v_and_b32_e32 v245, 0xffff0000, v52
	v_fmac_f32_e32 v99, v141, v141
	v_mfma_f32_32x32x2_f32 v[0:15], v46, v142, v[0:15]
	v_lshlrev_b32_e32 v246, 16, v53
	v_fmac_f32_e32 v99, v142, v142
	v_mfma_f32_32x32x2_f32 v[0:15], v47, v143, v[0:15]
	v_and_b32_e32 v247, 0xffff0000, v53
	v_fmac_f32_e32 v99, v143, v143
	v_mfma_f32_32x32x2_f32 v[0:15], v48, v144, v[0:15]
	v_lshlrev_b32_e32 v248, 16, v54
	v_fmac_f32_e32 v99, v144, v144
	v_mfma_f32_32x32x2_f32 v[0:15], v49, v145, v[0:15]
	v_and_b32_e32 v249, 0xffff0000, v54
	v_fmac_f32_e32 v99, v145, v145
	v_mfma_f32_32x32x2_f32 v[0:15], v50, v146, v[0:15]
	v_lshlrev_b32_e32 v250, 16, v55
	v_fmac_f32_e32 v99, v146, v146
	v_mfma_f32_32x32x2_f32 v[0:15], v51, v147, v[0:15]
	v_and_b32_e32 v251, 0xffff0000, v55
	v_fmac_f32_e32 v99, v147, v147
	s_waitcnt vmcnt(9)
	v_mfma_f32_32x32x2_f32 v[0:15], v56, v244, v[0:15]
	v_lshlrev_b32_e32 v140, 16, v64
	v_fmac_f32_e32 v99, v244, v244
	v_mfma_f32_32x32x2_f32 v[0:15], v57, v245, v[0:15]
	v_and_b32_e32 v141, 0xffff0000, v64
	v_fmac_f32_e32 v99, v245, v245
	v_mfma_f32_32x32x2_f32 v[0:15], v58, v246, v[0:15]
	v_lshlrev_b32_e32 v142, 16, v65
	v_fmac_f32_e32 v99, v246, v246
	v_mfma_f32_32x32x2_f32 v[0:15], v59, v247, v[0:15]
	v_and_b32_e32 v143, 0xffff0000, v65
	v_fmac_f32_e32 v99, v247, v247
	v_mfma_f32_32x32x2_f32 v[0:15], v60, v248, v[0:15]
	v_lshlrev_b32_e32 v144, 16, v66
	v_fmac_f32_e32 v99, v248, v248
	v_mfma_f32_32x32x2_f32 v[0:15], v61, v249, v[0:15]
	v_and_b32_e32 v145, 0xffff0000, v66
	v_fmac_f32_e32 v99, v249, v249
	v_mfma_f32_32x32x2_f32 v[0:15], v62, v250, v[0:15]
	v_lshlrev_b32_e32 v146, 16, v67
	v_fmac_f32_e32 v99, v250, v250
	v_mfma_f32_32x32x2_f32 v[0:15], v63, v251, v[0:15]
	v_and_b32_e32 v147, 0xffff0000, v67
	v_fmac_f32_e32 v99, v251, v251
	s_waitcnt vmcnt(6)
	v_mfma_f32_32x32x2_f32 v[0:15], v68, v140, v[0:15]
	v_lshlrev_b32_e32 v244, 16, v76
	v_fmac_f32_e32 v99, v140, v140
	v_mfma_f32_32x32x2_f32 v[0:15], v69, v141, v[0:15]
	v_and_b32_e32 v245, 0xffff0000, v76
	v_fmac_f32_e32 v99, v141, v141
	v_mfma_f32_32x32x2_f32 v[0:15], v70, v142, v[0:15]
	v_lshlrev_b32_e32 v246, 16, v77
	v_fmac_f32_e32 v99, v142, v142
	v_mfma_f32_32x32x2_f32 v[0:15], v71, v143, v[0:15]
	v_and_b32_e32 v247, 0xffff0000, v77
	v_fmac_f32_e32 v99, v143, v143
	v_mfma_f32_32x32x2_f32 v[0:15], v72, v144, v[0:15]
	v_lshlrev_b32_e32 v248, 16, v78
	v_fmac_f32_e32 v99, v144, v144
	v_mfma_f32_32x32x2_f32 v[0:15], v73, v145, v[0:15]
	v_and_b32_e32 v249, 0xffff0000, v78
	v_fmac_f32_e32 v99, v145, v145
	v_mfma_f32_32x32x2_f32 v[0:15], v74, v146, v[0:15]
	v_lshlrev_b32_e32 v250, 16, v79
	v_fmac_f32_e32 v99, v146, v146
	v_mfma_f32_32x32x2_f32 v[0:15], v75, v147, v[0:15]
	v_and_b32_e32 v251, 0xffff0000, v79
	v_fmac_f32_e32 v99, v147, v147
	s_waitcnt vmcnt(3)
; #define LAS __attribute__((address_space(3)))
; __device__ __forceinline__ float bf_lo(unsigned w) { return __uint_as_float(w << 16); }
; __device__ __forceinline__ float bf_hi(unsigned w) { return __uint_as_float(w & 0xffff0000u); }
; __global__ void __launch_bounds__(512, 2) fwd_kernel(Params p) {
;     ...
; #pragma unroll
;                     for (int i = 0; i < 8; ++i) { const u32x2 xp = xb[ch & 1][i]; const f32x4 xv = {bf_lo(xp.x), bf_hi(xp.x), bf_lo(xp.y), bf_hi(xp.y)}, wv = wb[ch & 1][i];
;                         acc = __builtin_amdgcn_mfma_f32_32x32x2f32(wv.x, xv.x, acc, 0, 0, 0); acc = __builtin_amdgcn_mfma_f32_32x32x2f32(wv.y, xv.y, acc, 0, 0, 0);
;                         acc = __builtin_amdgcn_mfma_f32_32x32x2f32(wv.z, xv.z, acc, 0, 0, 0); acc = __builtin_amdgcn_mfma_f32_32x32x2f32(wv.w, xv.w, acc, 0, 0, 0);
;                         ss += (xv.x * xv.x + xv.y * xv.y) + (xv.z * xv.z + xv.w * xv.w); }
;                 }
;                 LAS float* pp = part + ((kq * 2 + tt) * 32 + j) * 33;
; #pragma unroll
;                 for (int r = 0; r < 16; ++r) pp[(r & 3) + 8 * (r >> 2) + 4 * hh] = acc[r];
;                 ssq[((kq * 2 + tt) * 32 + j) * 2 + hh] = ss;
;             }
;             __syncthreads();
;             int te[4];
;             if (tid < 64) {
;                 const int t2 = tid >> 5, jj = tid & 31, tok = blk * 64 + tid;
;                 float s = 0.f;
; #pragma unroll
;                 for (int q = 0; q < 4; ++q) s += ssq[((q * 2 + t2) * 32 + jj) * 2] + ssq[((q * 2 + t2) * 32 + jj) * 2 + 1];
;                 const float rstd = rsqrtf(s * (1.f / DM) + RMS_EPS);
;                 RS2[tok] = rstd;
	v_mfma_f32_32x32x2_f32 v[0:15], v80, v244, v[0:15]
	v_lshlrev_b32_e32 v140, 16, v108
	v_fmac_f32_e32 v99, v244, v244
	v_mfma_f32_32x32x2_f32 v[0:15], v81, v245, v[0:15]
	v_and_b32_e32 v141, 0xffff0000, v108
	v_fmac_f32_e32 v99, v245, v245
	v_mfma_f32_32x32x2_f32 v[0:15], v82, v246, v[0:15]
	v_lshlrev_b32_e32 v142, 16, v109
	v_fmac_f32_e32 v99, v246, v246
	v_mfma_f32_32x32x2_f32 v[0:15], v83, v247, v[0:15]
	v_and_b32_e32 v143, 0xffff0000, v109
	v_fmac_f32_e32 v99, v247, v247
	v_mfma_f32_32x32x2_f32 v[0:15], v104, v248, v[0:15]
	v_lshlrev_b32_e32 v144, 16, v110
	v_fmac_f32_e32 v99, v248, v248
	v_mfma_f32_32x32x2_f32 v[0:15], v105, v249, v[0:15]
	v_and_b32_e32 v145, 0xffff0000, v110
	v_fmac_f32_e32 v99, v249, v249
	v_mfma_f32_32x32x2_f32 v[0:15], v106, v250, v[0:15]
	v_lshlrev_b32_e32 v146, 16, v111
	v_fmac_f32_e32 v99, v250, v250
	v_mfma_f32_32x32x2_f32 v[0:15], v107, v251, v[0:15]
	v_and_b32_e32 v147, 0xffff0000, v111
	v_fmac_f32_e32 v99, v251, v251
	s_waitcnt vmcnt(0)
	v_mfma_f32_32x32x2_f32 v[0:15], v112, v140, v[0:15]
	v_lshlrev_b32_e32 v244, 16, v120
	v_fmac_f32_e32 v99, v140, v140
	v_mfma_f32_32x32x2_f32 v[0:15], v113, v141, v[0:15]
	v_and_b32_e32 v245, 0xffff0000, v120
	v_fmac_f32_e32 v99, v141, v141
	v_mfma_f32_32x32x2_f32 v[0:15], v114, v142, v[0:15]
	v_lshlrev_b32_e32 v246, 16, v121
	v_fmac_f32_e32 v99, v142, v142
	v_mfma_f32_32x32x2_f32 v[0:15], v115, v143, v[0:15]
	v_and_b32_e32 v247, 0xffff0000, v121
	v_fmac_f32_e32 v99, v143, v143
	v_mfma_f32_32x32x2_f32 v[0:15], v116, v144, v[0:15]
	v_lshlrev_b32_e32 v248, 16, v122
	v_fmac_f32_e32 v99, v144, v144
	v_mfma_f32_32x32x2_f32 v[0:15], v117, v145, v[0:15]
	v_and_b32_e32 v249, 0xffff0000, v122
	v_fmac_f32_e32 v99, v145, v145
	v_mfma_f32_32x32x2_f32 v[0:15], v118, v146, v[0:15]
	v_lshlrev_b32_e32 v250, 16, v123
	v_fmac_f32_e32 v99, v146, v146
	v_mfma_f32_32x32x2_f32 v[0:15], v119, v147, v[0:15]
	v_and_b32_e32 v251, 0xffff0000, v123
	v_fmac_f32_e32 v99, v147, v147
	v_mfma_f32_32x32x2_f32 v[0:15], v124, v244, v[0:15]
	v_fmac_f32_e32 v99, v244, v244
	v_mfma_f32_32x32x2_f32 v[0:15], v125, v245, v[0:15]
	v_fmac_f32_e32 v99, v245, v245
	v_mfma_f32_32x32x2_f32 v[0:15], v126, v246, v[0:15]
	v_fmac_f32_e32 v99, v246, v246
	v_mfma_f32_32x32x2_f32 v[0:15], v127, v247, v[0:15]
	v_fmac_f32_e32 v99, v247, v247
	v_mfma_f32_32x32x2_f32 v[0:15], v128, v248, v[0:15]
	v_fmac_f32_e32 v99, v248, v248
	v_mfma_f32_32x32x2_f32 v[0:15], v129, v249, v[0:15]
	v_fmac_f32_e32 v99, v249, v249
	v_mfma_f32_32x32x2_f32 v[0:15], v130, v250, v[0:15]
	v_fmac_f32_e32 v99, v250, v250
	v_mfma_f32_32x32x2_f32 v[0:15], v131, v251, v[0:15]
	v_fmac_f32_e32 v99, v251, v251
	s_nop 15
	s_nop 1
	ds_write2_b32 v85, v0, v1 offset1:1
	ds_write2_b32 v85, v2, v3 offset0:2 offset1:3
	ds_write2_b32 v85, v4, v5 offset0:8 offset1:9
	ds_write2_b32 v85, v6, v7 offset0:10 offset1:11
	ds_write2_b32 v85, v8, v9 offset0:16 offset1:17
	ds_write2_b32 v85, v10, v11 offset0:18 offset1:19
	ds_write2_b32 v85, v12, v13 offset0:24 offset1:25
	ds_write2_b32 v85, v14, v15 offset0:26 offset1:27
	v_mov_b32_e32 v0, v99
	v_add_u32_e32 v34, s10, v84
	v_ashrrev_i32_e32 v35, 31, v34
	ds_write_b32 v86, v0 offset:36864
	global_load_dwordx4 v[200:203], v87, s[38:39] offset:48
	global_load_dwordx4 v[204:207], v87, s[38:39] offset:32
	global_load_dwordx4 v[208:211], v87, s[38:39] offset:16
	global_load_dwordx4 v[212:215], v87, s[38:39]
	global_load_dwordx4 v[216:219], v87, s[38:39] offset:112
	global_load_dwordx4 v[220:223], v87, s[38:39] offset:96
	global_load_dwordx4 v[224:227], v87, s[38:39] offset:80
	global_load_dwordx4 v[228:231], v87, s[38:39] offset:64
	s_waitcnt lgkmcnt(0)
	s_barrier
	s_and_saveexec_b64 s[46:47], s[6:7]
	s_cbranch_execz .LBB0_986
	ds_read2st64_b64 v[0:3], v136 offset0:72 offset1:73
	ds_read2_b32 v[18:19], v135 offset1:1
	s_movk_i32 s0, 0x80
	s_waitcnt lgkmcnt(1)
	v_mov_b32_e32 v4, v0
	v_mov_b32_e32 v5, v2
	v_mov_b32_e32 v2, v1
	v_pk_add_f32 v[0:1], v[4:5], v[2:3]
	s_nop 0
	v_add_f32_e32 v0, 0, v0
	v_add_f32_e32 v6, v0, v1
	ds_read2st64_b64 v[0:3], v136 offset0:74 offset1:75
	s_waitcnt lgkmcnt(0)
	v_mov_b32_e32 v4, v0
	v_mov_b32_e32 v5, v2
	v_mov_b32_e32 v2, v1
	v_pk_add_f32 v[0:1], v[4:5], v[2:3]
	s_nop 0
	v_add_f32_e32 v0, v6, v0
	v_add_f32_e32 v0, v0, v1
	v_fmamk_f32 v0, v0, 0x3a000000, v137
	v_cmp_gt_f32_e32 vcc, s57, v0
	v_mul_f32_e32 v1, 0x4b800000, v0
	s_nop 0
	v_cndmask_b32_e32 v0, v0, v1, vcc
	v_rsq_f32_e32 v0, v0
	s_nop 0
	v_mul_f32_e32 v1, 0x45800000, v0
	v_cndmask_b32_e32 v16, v0, v1, vcc
	v_mov_b32_e32 v244, v16
	v_lshl_add_u64 v[0:1], v[34:35], 2, s[44:45]
	global_store_dword v[0:1], v16, off
	v_add_u32_e32 v1, 0x2100, v135
	ds_read2_b32 v[20:21], v1 offset1:1
	v_add_u32_e32 v1, 0x4200, v135
	ds_read2_b32 v[22:23], v1 offset1:1
	v_add_u32_e32 v1, 0x6300, v135
	ds_read2_b32 v[24:25], v1 offset1:1
	v_add_f32_e32 v0, 0, v18
	s_waitcnt lgkmcnt(2)
	v_add_f32_e32 v0, v0, v20
	s_waitcnt lgkmcnt(1)
	v_add_f32_e32 v0, v0, v22
	s_waitcnt lgkmcnt(0)
	v_add_f32_e32 v17, v0, v24
	s_waitcnt vmcnt(1)
	v_mov_b32_e32 v0, v200
	v_mov_b32_e32 v1, v201
	v_mov_b32_e32 v2, v202
	v_mov_b32_e32 v3, v203
	v_mov_b32_e32 v4, v204
	v_mov_b32_e32 v5, v205
	v_mov_b32_e32 v6, v206
	v_mov_b32_e32 v7, v207
	v_mov_b32_e32 v8, v208
	v_mov_b32_e32 v9, v209
	v_mov_b32_e32 v10, v210
	v_mov_b32_e32 v11, v211
	v_mov_b32_e32 v12, v212
	v_mov_b32_e32 v13, v213
	v_mov_b32_e32 v14, v214
	v_mov_b32_e32 v15, v215
	v_fma_f32 v37, v16, v17, v12
	v_add_f32_e32 v12, 0, v19
	v_add_f32_e32 v12, v12, v21
	v_add_f32_e32 v12, v12, v23
	v_add_f32_e32 v12, v12, v25
	v_fma_f32 v36, v16, v12, v13
	ds_read2_b32 v[12:13], v135 offset0:2 offset1:3
	v_add_u32_e32 v17, 0x2108, v135
	ds_read2_b32 v[18:19], v17 offset1:1
	v_add_u32_e32 v17, 0x4208, v135
	ds_read2_b32 v[20:21], v17 offset1:1
	v_add_u32_e32 v17, 0x6308, v135
	ds_read2_b32 v[22:23], v17 offset1:1
	s_waitcnt lgkmcnt(3)
; __global__ void __launch_bounds__(512, 2) fwd_kernel(Params p) {
;     ...
;                 float lgv[NE];
; #pragma unroll
;                 for (int e = 0; e < NE; ++e) { float v = 0.f;
; #pragma unroll
;                     for (int q = 0; q < 4; ++q) v += part[((q * 2 + t2) * 32 + jj) * 33 + e];
;                     lgv[e] = v * rstd + p.in[I_BR][e]; }
	v_add_f32_e32 v12, 0, v12
	s_waitcnt lgkmcnt(2)
	v_add_f32_e32 v12, v12, v18
	s_waitcnt lgkmcnt(1)
	v_add_f32_e32 v12, v12, v20
	v_add_u32_e32 v17, 0x2110, v135
	s_waitcnt lgkmcnt(0)
	v_add_f32_e32 v12, v12, v22
	v_fma_f32 v14, v16, v12, v14
	v_add_f32_e32 v12, 0, v13
	v_add_f32_e32 v12, v12, v19
	v_add_f32_e32 v12, v12, v21
	v_add_f32_e32 v12, v12, v23
	v_fmac_f32_e32 v15, v16, v12
	ds_read2_b32 v[12:13], v135 offset0:4 offset1:5
	ds_read2_b32 v[18:19], v17 offset1:1
	v_add_u32_e32 v17, 0x4210, v135
	ds_read2_b32 v[20:21], v17 offset1:1
	v_add_u32_e32 v17, 0x6310, v135
	ds_read2_b32 v[22:23], v17 offset1:1
	s_waitcnt lgkmcnt(3)
	v_add_f32_e32 v12, 0, v12
	s_waitcnt lgkmcnt(2)
	v_add_f32_e32 v12, v12, v18
	s_waitcnt lgkmcnt(1)
	v_add_f32_e32 v12, v12, v20
	v_cmp_lg_f32_e32 vcc, s58, v37
	s_waitcnt lgkmcnt(0)
	v_add_f32_e32 v12, v12, v22
	v_fma_f32 v39, v16, v12, v8
	v_add_f32_e32 v8, 0, v13
	v_add_f32_e32 v8, v8, v19
	v_add_f32_e32 v8, v8, v21
	v_add_f32_e32 v8, v8, v23
	v_fma_f32 v38, v16, v8, v9
	ds_read2_b32 v[8:9], v135 offset0:6 offset1:7
	v_add_u32_e32 v12, 0x2118, v135
	ds_read2_b32 v[12:13], v12 offset1:1
	s_waitcnt lgkmcnt(1)
	v_add_f32_e32 v8, 0, v8
	s_waitcnt lgkmcnt(0)
	v_add_f32_e32 v8, v8, v12
	v_add_u32_e32 v12, 0x4218, v135
	ds_read2_b32 v[18:19], v12 offset1:1
	v_add_u32_e32 v12, 0x6318, v135
	ds_read2_b32 v[20:21], v12 offset1:1
	v_add_u32_e32 v12, 0x2120, v135
	s_waitcnt lgkmcnt(1)
	v_add_f32_e32 v8, v8, v18
	s_waitcnt lgkmcnt(0)
	v_add_f32_e32 v8, v8, v20
	v_fma_f32 v10, v16, v8, v10
	v_add_f32_e32 v8, 0, v9
	v_add_f32_e32 v8, v8, v13
	v_add_f32_e32 v8, v8, v19
	v_add_f32_e32 v8, v8, v21
	v_fmac_f32_e32 v11, v16, v8
	ds_read2_b32 v[8:9], v135 offset0:8 offset1:9
	ds_read2_b32 v[12:13], v12 offset1:1
	s_waitcnt lgkmcnt(1)
	v_add_f32_e32 v8, 0, v8
	s_waitcnt lgkmcnt(0)
	v_add_f32_e32 v8, v8, v12
	v_add_u32_e32 v12, 0x4220, v135
	ds_read2_b32 v[18:19], v12 offset1:1
	v_add_u32_e32 v12, 0x6320, v135
	ds_read2_b32 v[20:21], v12 offset1:1
	s_waitcnt lgkmcnt(1)
	v_add_f32_e32 v8, v8, v18
	s_waitcnt lgkmcnt(0)
	v_add_f32_e32 v8, v8, v20
	v_fma_f32 v41, v16, v8, v4
	v_add_f32_e32 v4, 0, v9
	v_add_f32_e32 v4, v4, v13
	v_add_f32_e32 v4, v4, v19
	v_add_f32_e32 v4, v4, v21
	v_fma_f32 v40, v16, v4, v5
	ds_read2_b32 v[4:5], v135 offset0:10 offset1:11
	v_add_u32_e32 v8, 0x2128, v135
	ds_read2_b32 v[8:9], v8 offset1:1
	s_waitcnt lgkmcnt(1)
	v_add_f32_e32 v4, 0, v4
	s_waitcnt lgkmcnt(0)
	v_add_f32_e32 v4, v4, v8
	v_add_u32_e32 v8, 0x4228, v135
	ds_read2_b32 v[12:13], v8 offset1:1
	v_add_u32_e32 v8, 0x6328, v135
	ds_read2_b32 v[18:19], v8 offset1:1
	v_add_u32_e32 v8, 0x2130, v135
	s_waitcnt lgkmcnt(1)
	v_add_f32_e32 v4, v4, v12
	s_waitcnt lgkmcnt(0)
	v_add_f32_e32 v4, v4, v18
	v_fma_f32 v6, v16, v4, v6
	v_add_f32_e32 v4, 0, v5
	v_add_f32_e32 v4, v4, v9
	v_add_f32_e32 v4, v4, v13
	v_add_f32_e32 v4, v4, v19
	v_fmac_f32_e32 v7, v16, v4
	ds_read2_b32 v[4:5], v135 offset0:12 offset1:13
	ds_read2_b32 v[8:9], v8 offset1:1
	s_waitcnt lgkmcnt(1)
	v_add_f32_e32 v4, 0, v4
	s_waitcnt lgkmcnt(0)
	v_add_f32_e32 v4, v4, v8
	v_add_u32_e32 v8, 0x4230, v135
	ds_read2_b32 v[12:13], v8 offset1:1
	v_add_u32_e32 v8, 0x6330, v135
	ds_read2_b32 v[18:19], v8 offset1:1
	s_waitcnt lgkmcnt(1)
	v_add_f32_e32 v4, v4, v12
	s_waitcnt lgkmcnt(0)
	v_add_f32_e32 v4, v4, v18
	v_fma_f32 v43, v16, v4, v0
	v_add_f32_e32 v0, 0, v5
	v_add_f32_e32 v0, v0, v9
	v_add_f32_e32 v0, v0, v13
	v_add_f32_e32 v0, v0, v19
	v_fma_f32 v42, v16, v0, v1
	ds_read2_b32 v[0:1], v135 offset0:14 offset1:15
	v_add_u32_e32 v4, 0x2138, v135
	ds_read2_b32 v[4:5], v4 offset1:1
	s_waitcnt lgkmcnt(1)
	v_add_f32_e32 v0, 0, v0
	s_waitcnt lgkmcnt(0)
	v_add_f32_e32 v0, v0, v4
	v_add_u32_e32 v4, 0x4238, v135
	ds_read2_b32 v[8:9], v4 offset1:1
	v_add_u32_e32 v4, 0x6338, v135
	ds_read2_b32 v[12:13], v4 offset1:1
	v_add_u32_e32 v4, 0x2140, v135
	s_waitcnt lgkmcnt(1)
	v_add_f32_e32 v0, v0, v8
	s_waitcnt lgkmcnt(0)
	v_add_f32_e32 v0, v0, v12
	v_fma_f32 v2, v16, v0, v2
	v_add_f32_e32 v0, 0, v1
	v_add_f32_e32 v0, v0, v5
	v_add_f32_e32 v0, v0, v9
	v_add_f32_e32 v0, v0, v13
	v_fmac_f32_e32 v3, v16, v0
	ds_read2_b32 v[0:1], v135 offset0:16 offset1:17
	ds_read2_b32 v[4:5], v4 offset1:1
	s_waitcnt lgkmcnt(1)
	v_add_f32_e32 v0, 0, v0
	s_waitcnt lgkmcnt(0)
	v_add_f32_e32 v0, v0, v4
	v_add_u32_e32 v4, 0x4240, v135
	ds_read2_b32 v[8:9], v4 offset1:1
	v_add_u32_e32 v4, 0x6340, v135
	ds_read2_b32 v[12:13], v4 offset1:1
	v_mov_b32_e32 v18, v216
	v_mov_b32_e32 v19, v217
	v_mov_b32_e32 v20, v218
	v_mov_b32_e32 v21, v219
	v_mov_b32_e32 v22, v220
	v_mov_b32_e32 v23, v221
	v_mov_b32_e32 v24, v222
	v_mov_b32_e32 v25, v223
	v_mov_b32_e32 v26, v224
	v_mov_b32_e32 v27, v225
	v_mov_b32_e32 v28, v226
	v_mov_b32_e32 v29, v227
	v_mov_b32_e32 v30, v228
	v_mov_b32_e32 v31, v229
	v_mov_b32_e32 v32, v230
	v_mov_b32_e32 v33, v231
	s_waitcnt lgkmcnt(1)
	v_add_f32_e32 v0, v0, v8
	s_waitcnt lgkmcnt(0)
	v_add_f32_e32 v0, v0, v12
	v_fma_f32 v4, v16, v0, v30
	v_add_f32_e32 v0, 0, v1
	v_add_f32_e32 v0, v0, v5
	v_add_f32_e32 v0, v0, v9
	ds_read2_b32 v[8:9], v135 offset0:18 offset1:19
	v_add_u32_e32 v5, 0x2148, v135
	v_add_f32_e32 v0, v0, v13
	ds_read2_b32 v[12:13], v5 offset1:1
	v_add_u32_e32 v5, 0x4248, v135
	v_fma_f32 v0, v16, v0, v31
	ds_read2_b32 v[30:31], v5 offset1:1
	v_add_u32_e32 v5, 0x6348, v135
	ds_read2_b32 v[44:45], v5 offset1:1
	s_waitcnt lgkmcnt(3)
	v_add_f32_e32 v1, 0, v8
	v_add_f32_e32 v5, 0, v9
	ds_read2_b32 v[8:9], v135 offset0:20 offset1:21
	s_waitcnt lgkmcnt(3)
	v_add_f32_e32 v5, v5, v13
	s_waitcnt lgkmcnt(2)
	v_add_f32_e32 v5, v5, v31
	s_waitcnt lgkmcnt(1)
	v_add_f32_e32 v5, v5, v45
	v_fmac_f32_e32 v33, v16, v5
	s_waitcnt lgkmcnt(0)
; __global__ void __launch_bounds__(512, 2) fwd_kernel(Params p) {
;     ...
;                 float lgv[NE];
; #pragma unroll
;                 for (int e = 0; e < NE; ++e) { float v = 0.f;
; #pragma unroll
;                     for (int q = 0; q < 4; ++q) v += part[((q * 2 + t2) * 32 + jj) * 33 + e];
;                     lgv[e] = v * rstd + p.in[I_BR][e]; }
;                 unsigned mask = 0u; float tv[4];
; #pragma unroll
;                 for (int k = 0; k < 4; ++k) { float best = -__builtin_inff(); int be = 0;
; #pragma unroll
;                     for (int e = 0; e < NE; ++e) { const bool take = !((mask >> e) & 1u) && lgv[e] > best; best = take ? lgv[e] : best; be = take ? e : be; }
;                     mask |= 1u << be; tv[k] = best; te[k] = be; }
	v_add_f32_e32 v5, 0, v8
	v_add_u32_e32 v8, 0x2150, v135
	v_add_f32_e32 v1, v1, v12
	ds_read2_b32 v[12:13], v8 offset1:1
	v_add_u32_e32 v8, 0x4250, v135
	v_add_f32_e32 v1, v1, v30
	ds_read2_b32 v[30:31], v8 offset1:1
	v_add_u32_e32 v8, 0x6350, v135
	v_add_f32_e32 v1, v1, v44
	ds_read2_b32 v[44:45], v8 offset1:1
	s_waitcnt lgkmcnt(2)
	v_add_f32_e32 v5, v5, v12
	s_waitcnt lgkmcnt(1)
	v_add_f32_e32 v5, v5, v30
	v_fma_f32 v1, v16, v1, v32
	s_waitcnt lgkmcnt(0)
	v_add_f32_e32 v5, v5, v44
	v_fma_f32 v8, v16, v5, v26
	v_add_f32_e32 v5, 0, v9
	v_add_f32_e32 v5, v5, v13
	ds_read2_b32 v[12:13], v135 offset0:22 offset1:23
	v_add_f32_e32 v5, v5, v31
	v_add_f32_e32 v5, v5, v45
	v_fma_f32 v5, v16, v5, v27
	s_waitcnt lgkmcnt(0)
	v_add_f32_e32 v9, 0, v12
	v_add_u32_e32 v12, 0x2158, v135
	ds_read2_b32 v[26:27], v12 offset1:1
	v_add_u32_e32 v12, 0x4258, v135
	ds_read2_b32 v[30:31], v12 offset1:1
	v_add_u32_e32 v12, 0x6358, v135
	ds_read2_b32 v[44:45], v12 offset1:1
	v_add_f32_e32 v12, 0, v13
	s_waitcnt lgkmcnt(2)
	v_add_f32_e32 v9, v9, v26
	v_add_f32_e32 v12, v12, v27
	ds_read2_b32 v[26:27], v135 offset0:24 offset1:25
	v_add_u32_e32 v13, 0x2160, v135
	s_waitcnt lgkmcnt(2)
	v_add_f32_e32 v9, v9, v30
	v_add_f32_e32 v12, v12, v31
	ds_read2_b32 v[30:31], v13 offset1:1
	v_add_u32_e32 v13, 0x4260, v135
	s_waitcnt lgkmcnt(2)
	v_add_f32_e32 v9, v9, v44
	v_add_f32_e32 v12, v12, v45
	ds_read2_b32 v[44:45], v13 offset1:1
	v_add_u32_e32 v13, 0x6360, v135
	ds_read2_b32 v[46:47], v13 offset1:1
	v_fmac_f32_e32 v29, v16, v12
	s_waitcnt lgkmcnt(3)
	v_add_f32_e32 v12, 0, v26
	s_waitcnt lgkmcnt(2)
	v_add_f32_e32 v12, v12, v30
	s_waitcnt lgkmcnt(1)
	v_add_f32_e32 v12, v12, v44
	s_waitcnt lgkmcnt(0)
	v_add_f32_e32 v12, v12, v46
	v_fma_f32 v13, v16, v12, v22
	v_add_f32_e32 v12, 0, v27
	v_add_f32_e32 v12, v12, v31
	v_add_f32_e32 v12, v12, v45
	v_add_f32_e32 v12, v12, v47
	v_fma_f32 v12, v16, v12, v23
	ds_read2_b32 v[22:23], v135 offset0:26 offset1:27
	v_fma_f32 v9, v16, v9, v28
	s_waitcnt lgkmcnt(0)
	v_add_f32_e32 v17, 0, v22
	v_add_u32_e32 v22, 0x2168, v135
	ds_read2_b32 v[26:27], v22 offset1:1
	v_add_u32_e32 v22, 0x4268, v135
	ds_read2_b32 v[30:31], v22 offset1:1
	v_add_u32_e32 v22, 0x6368, v135
	ds_read2_b32 v[44:45], v22 offset1:1
	s_waitcnt lgkmcnt(2)
	v_add_f32_e32 v17, v17, v26
	s_waitcnt lgkmcnt(1)
	v_add_f32_e32 v17, v17, v30
	s_waitcnt lgkmcnt(0)
	v_add_f32_e32 v17, v17, v44
	v_fma_f32 v22, v16, v17, v24
	v_add_f32_e32 v17, 0, v23
	v_add_f32_e32 v17, v17, v27
	ds_read2_b32 v[26:27], v135 offset0:28 offset1:29
	v_add_u32_e32 v23, 0x2170, v135
	v_add_f32_e32 v17, v17, v31
	ds_read2_b32 v[30:31], v23 offset1:1
	v_add_u32_e32 v23, 0x4270, v135
	v_add_f32_e32 v17, v17, v45
	ds_read2_b32 v[44:45], v23 offset1:1
	v_add_u32_e32 v23, 0x6370, v135
	ds_read2_b32 v[46:47], v23 offset1:1
	v_fmac_f32_e32 v25, v16, v17
	s_waitcnt lgkmcnt(3)
	v_add_f32_e32 v17, 0, v26
	s_waitcnt lgkmcnt(2)
	v_add_f32_e32 v17, v17, v30
	s_waitcnt lgkmcnt(1)
	v_add_f32_e32 v17, v17, v44
	s_waitcnt lgkmcnt(0)
	v_add_f32_e32 v17, v17, v46
	v_fma_f32 v23, v16, v17, v18
	v_add_f32_e32 v17, 0, v27
	ds_read2_b32 v[26:27], v135 offset0:30 offset1:31
	v_add_u32_e32 v18, 0x2178, v135
	v_add_f32_e32 v17, v17, v31
	ds_read2_b32 v[30:31], v18 offset1:1
	v_add_u32_e32 v18, 0x4278, v135
	v_add_f32_e32 v17, v17, v45
	ds_read2_b32 v[44:45], v18 offset1:1
	v_add_u32_e32 v18, 0x6378, v135
	v_add_f32_e32 v17, v17, v47
	ds_read2_b32 v[46:47], v18 offset1:1
	v_fma_f32 v19, v16, v17, v19
	s_waitcnt lgkmcnt(3)
	v_add_f32_e32 v17, 0, v26
	s_waitcnt lgkmcnt(2)
	v_add_f32_e32 v17, v17, v30
	s_waitcnt lgkmcnt(1)
	v_add_f32_e32 v17, v17, v44
	s_waitcnt lgkmcnt(0)
	v_add_f32_e32 v17, v17, v46
	v_fma_f32 v20, v16, v17, v20
	v_add_f32_e32 v17, 0, v27
	v_add_f32_e32 v17, v17, v31
	v_add_f32_e32 v17, v17, v45
	v_add_f32_e32 v17, v17, v47
	v_fmac_f32_e32 v21, v16, v17
	v_cndmask_b32_e32 v16, v139, v37, vcc
	v_cmp_gt_f32_e32 vcc, v36, v16
	s_nop 1
	v_cndmask_b32_e32 v16, v16, v36, vcc
	v_cndmask_b32_e64 v17, 0, 1, vcc
	v_cmp_gt_f32_e32 vcc, v14, v16
	s_nop 1
	v_cndmask_b32_e32 v16, v16, v14, vcc
	v_cndmask_b32_e64 v17, v17, 2, vcc
	v_cmp_gt_f32_e32 vcc, v15, v16
	s_nop 1
	v_cndmask_b32_e32 v16, v16, v15, vcc
	v_cndmask_b32_e64 v17, v17, 3, vcc
	v_cmp_gt_f32_e32 vcc, v39, v16
	s_nop 1
	v_cndmask_b32_e32 v16, v16, v39, vcc
	v_cndmask_b32_e64 v17, v17, 4, vcc
	v_cmp_gt_f32_e32 vcc, v38, v16
	s_nop 1
	v_cndmask_b32_e32 v16, v16, v38, vcc
	v_cndmask_b32_e64 v17, v17, 5, vcc
	v_cmp_gt_f32_e32 vcc, v10, v16
	s_nop 1
	v_cndmask_b32_e32 v16, v16, v10, vcc
	v_cndmask_b32_e64 v17, v17, 6, vcc
	v_cmp_gt_f32_e32 vcc, v11, v16
	s_nop 1
	v_cndmask_b32_e32 v16, v16, v11, vcc
	v_cndmask_b32_e64 v17, v17, 7, vcc
	v_cmp_gt_f32_e32 vcc, v41, v16
	s_nop 1
	v_cndmask_b32_e32 v16, v16, v41, vcc
	v_cndmask_b32_e64 v17, v17, 8, vcc
	v_cmp_gt_f32_e32 vcc, v40, v16
	s_nop 1
	v_cndmask_b32_e32 v16, v16, v40, vcc
	v_cndmask_b32_e64 v17, v17, 9, vcc
	v_cmp_gt_f32_e32 vcc, v6, v16
	s_nop 1
	v_cndmask_b32_e32 v16, v16, v6, vcc
	v_cndmask_b32_e64 v17, v17, 10, vcc
	v_cmp_gt_f32_e32 vcc, v7, v16
	s_nop 1
	v_cndmask_b32_e32 v16, v16, v7, vcc
	v_cndmask_b32_e64 v17, v17, 11, vcc
	v_cmp_gt_f32_e32 vcc, v43, v16
	s_nop 1
	v_cndmask_b32_e32 v16, v16, v43, vcc
	v_cndmask_b32_e64 v17, v17, 12, vcc
	v_cmp_gt_f32_e32 vcc, v42, v16
	s_nop 1
	v_cndmask_b32_e32 v16, v16, v42, vcc
	v_cndmask_b32_e64 v17, v17, 13, vcc
	v_cmp_gt_f32_e32 vcc, v2, v16
	s_nop 1
	v_cndmask_b32_e32 v16, v16, v2, vcc
	v_cndmask_b32_e64 v17, v17, 14, vcc
	v_cmp_gt_f32_e32 vcc, v3, v16
	s_nop 1
	v_cndmask_b32_e32 v16, v16, v3, vcc
	v_cndmask_b32_e64 v17, v17, 15, vcc
	v_cmp_gt_f32_e32 vcc, v4, v16
	s_nop 1
; __global__ void __launch_bounds__(512, 2) fwd_kernel(Params p) {
;     ...
;                 unsigned mask = 0u; float tv[4];
; #pragma unroll
;                 for (int k = 0; k < 4; ++k) { float best = -__builtin_inff(); int be = 0;
; #pragma unroll
;                     for (int e = 0; e < NE; ++e) { const bool take = !((mask >> e) & 1u) && lgv[e] > best; best = take ? lgv[e] : best; be = take ? e : be; }
;                     mask |= 1u << be; tv[k] = best; te[k] = be; }
	v_cndmask_b32_e32 v16, v16, v4, vcc
	v_cndmask_b32_e64 v17, v17, 16, vcc
	v_cmp_gt_f32_e32 vcc, v0, v16
	s_nop 1
	v_cndmask_b32_e32 v16, v16, v0, vcc
	v_cndmask_b32_e64 v17, v17, 17, vcc
	v_cmp_gt_f32_e32 vcc, v1, v16
	s_nop 1
	v_cndmask_b32_e32 v16, v16, v1, vcc
	v_cndmask_b32_e64 v17, v17, 18, vcc
	v_cmp_gt_f32_e32 vcc, v33, v16
	s_nop 1
	v_cndmask_b32_e32 v16, v16, v33, vcc
	v_cndmask_b32_e64 v17, v17, 19, vcc
	v_cmp_gt_f32_e32 vcc, v8, v16
	s_nop 1
	v_cndmask_b32_e32 v16, v16, v8, vcc
	v_cndmask_b32_e64 v17, v17, 20, vcc
	v_cmp_gt_f32_e32 vcc, v5, v16
	s_nop 1
	v_cndmask_b32_e32 v16, v16, v5, vcc
	v_cndmask_b32_e64 v17, v17, 21, vcc
	v_cmp_gt_f32_e32 vcc, v9, v16
	s_nop 1
	v_cndmask_b32_e32 v16, v16, v9, vcc
	v_cndmask_b32_e64 v17, v17, 22, vcc
	v_cmp_gt_f32_e32 vcc, v29, v16
	s_nop 1
	v_cndmask_b32_e32 v16, v16, v29, vcc
	v_cndmask_b32_e64 v17, v17, 23, vcc
	v_cmp_gt_f32_e32 vcc, v13, v16
	s_nop 1
	v_cndmask_b32_e32 v16, v16, v13, vcc
	v_cndmask_b32_e64 v17, v17, 24, vcc
	v_cmp_gt_f32_e32 vcc, v12, v16
	s_nop 1
	v_cndmask_b32_e32 v16, v16, v12, vcc
	v_cndmask_b32_e64 v17, v17, 25, vcc
	v_cmp_gt_f32_e32 vcc, v22, v16
	s_nop 1
	v_cndmask_b32_e32 v16, v16, v22, vcc
	v_cndmask_b32_e64 v17, v17, 26, vcc
	v_cmp_gt_f32_e32 vcc, v25, v16
	s_nop 1
	v_cndmask_b32_e32 v16, v16, v25, vcc
	v_cndmask_b32_e64 v17, v17, 27, vcc
	v_cmp_gt_f32_e32 vcc, v23, v16
	s_nop 1
	v_cndmask_b32_e32 v16, v16, v23, vcc
	v_cndmask_b32_e64 v17, v17, 28, vcc
	v_cmp_gt_f32_e32 vcc, v19, v16
	s_nop 1
	v_cndmask_b32_e32 v16, v16, v19, vcc
	v_cndmask_b32_e64 v17, v17, 29, vcc
	v_cmp_gt_f32_e32 vcc, v20, v16
	s_nop 1
	v_cndmask_b32_e32 v18, v16, v20, vcc
	v_cndmask_b32_e64 v17, v17, 30, vcc
	v_cmp_gt_f32_e32 vcc, v21, v18
	s_nop 1
	v_cndmask_b32_e64 v16, v17, 31, vcc
	v_cndmask_b32_e32 v24, v18, v21, vcc
	v_cmp_eq_u32_e64 s[10:11], 0, v16
	v_cmp_nlg_f32_e32 vcc, s58, v37
	v_lshlrev_b32_e64 v18, v16, 1
	s_or_b64 s[10:11], s[10:11], vcc
	v_cndmask_b32_e64 v17, v37, v139, s[10:11]
	v_and_b32_e32 v26, 2, v18
	v_cmp_eq_u32_e64 s[10:11], 0, v26
	v_cmp_gt_f32_e64 s[12:13], v36, v17
	s_and_b64 s[10:11], s[10:11], s[12:13]
	v_cndmask_b32_e64 v17, v17, v36, s[10:11]
	v_and_b32_e32 v27, 4, v18
	v_cndmask_b32_e64 v26, 0, 1, s[10:11]
	v_cmp_eq_u32_e64 s[10:11], 0, v27
	v_cmp_gt_f32_e64 s[12:13], v14, v17
	s_and_b64 s[10:11], s[10:11], s[12:13]
	v_cndmask_b32_e64 v17, v17, v14, s[10:11]
	v_and_b32_e32 v27, 8, v18
	v_cndmask_b32_e64 v26, v26, 2, s[10:11]
	v_cmp_eq_u32_e64 s[10:11], 0, v27
	v_cmp_gt_f32_e64 s[12:13], v15, v17
	s_and_b64 s[10:11], s[10:11], s[12:13]
	v_cndmask_b32_e64 v17, v17, v15, s[10:11]
	v_and_b32_e32 v27, 16, v18
	v_cndmask_b32_e64 v26, v26, 3, s[10:11]
	v_cmp_eq_u32_e64 s[10:11], 0, v27
	v_cmp_gt_f32_e64 s[12:13], v39, v17
	s_and_b64 s[10:11], s[10:11], s[12:13]
	v_cndmask_b32_e64 v17, v17, v39, s[10:11]
	v_and_b32_e32 v27, 32, v18
	v_cndmask_b32_e64 v26, v26, 4, s[10:11]
	v_cmp_eq_u32_e64 s[10:11], 0, v27
	v_cmp_gt_f32_e64 s[12:13], v38, v17
	s_and_b64 s[10:11], s[10:11], s[12:13]
	v_cndmask_b32_e64 v17, v17, v38, s[10:11]
	v_and_b32_e32 v27, 64, v18
	v_cndmask_b32_e64 v26, v26, 5, s[10:11]
	v_cmp_eq_u32_e64 s[10:11], 0, v27
	v_cmp_gt_f32_e64 s[12:13], v10, v17
	s_and_b64 s[10:11], s[10:11], s[12:13]
	v_cndmask_b32_e64 v17, v17, v10, s[10:11]
	v_and_b32_e32 v27, 0x80, v18
	v_cndmask_b32_e64 v26, v26, 6, s[10:11]
	v_cmp_eq_u32_e64 s[10:11], 0, v27
	v_cmp_gt_f32_e64 s[12:13], v11, v17
	s_and_b64 s[10:11], s[10:11], s[12:13]
	v_cndmask_b32_e64 v17, v17, v11, s[10:11]
	v_and_b32_e32 v27, 0x100, v18
	v_cndmask_b32_e64 v26, v26, 7, s[10:11]
	v_cmp_eq_u32_e64 s[10:11], 0, v27
	v_cmp_gt_f32_e64 s[12:13], v41, v17
	s_and_b64 s[10:11], s[10:11], s[12:13]
	v_cndmask_b32_e64 v17, v17, v41, s[10:11]
	v_and_b32_e32 v27, 0x200, v18
	v_cndmask_b32_e64 v26, v26, 8, s[10:11]
	v_cmp_eq_u32_e64 s[10:11], 0, v27
	v_cmp_gt_f32_e64 s[12:13], v40, v17
	s_and_b64 s[10:11], s[10:11], s[12:13]
	v_cndmask_b32_e64 v17, v17, v40, s[10:11]
	v_and_b32_e32 v27, 0x400, v18
	v_cndmask_b32_e64 v26, v26, 9, s[10:11]
	v_cmp_eq_u32_e64 s[10:11], 0, v27
	v_cmp_gt_f32_e64 s[12:13], v6, v17
	s_and_b64 s[10:11], s[10:11], s[12:13]
	v_cndmask_b32_e64 v17, v17, v6, s[10:11]
	v_and_b32_e32 v27, 0x800, v18
	v_cndmask_b32_e64 v26, v26, 10, s[10:11]
	v_cmp_eq_u32_e64 s[10:11], 0, v27
	v_cmp_gt_f32_e64 s[12:13], v7, v17
	s_and_b64 s[10:11], s[10:11], s[12:13]
	v_cndmask_b32_e64 v17, v17, v7, s[10:11]
	v_and_b32_e32 v27, 0x1000, v18
	v_cndmask_b32_e64 v26, v26, 11, s[10:11]
	v_cmp_eq_u32_e64 s[10:11], 0, v27
	v_cmp_gt_f32_e64 s[12:13], v43, v17
	s_and_b64 s[10:11], s[10:11], s[12:13]
	v_cndmask_b32_e64 v17, v17, v43, s[10:11]
	v_and_b32_e32 v27, 0x2000, v18
	v_cndmask_b32_e64 v26, v26, 12, s[10:11]
	v_cmp_eq_u32_e64 s[10:11], 0, v27
	v_cmp_gt_f32_e64 s[12:13], v42, v17
	s_and_b64 s[10:11], s[10:11], s[12:13]
	v_cndmask_b32_e64 v17, v17, v42, s[10:11]
	v_and_b32_e32 v27, 0x4000, v18
	v_cndmask_b32_e64 v26, v26, 13, s[10:11]
	v_cmp_eq_u32_e64 s[10:11], 0, v27
	v_cmp_gt_f32_e64 s[12:13], v2, v17
	s_and_b64 s[10:11], s[10:11], s[12:13]
	v_cndmask_b32_e64 v17, v17, v2, s[10:11]
	v_and_b32_e32 v27, 0x8000, v18
	v_cndmask_b32_e64 v26, v26, 14, s[10:11]
	v_cmp_eq_u32_e64 s[10:11], 0, v27
	v_cmp_gt_f32_e64 s[12:13], v3, v17
	s_and_b64 s[10:11], s[10:11], s[12:13]
	v_cndmask_b32_e64 v17, v17, v3, s[10:11]
	v_and_b32_e32 v27, 0x10000, v18
	v_cndmask_b32_e64 v26, v26, 15, s[10:11]
	v_cmp_eq_u32_e64 s[10:11], 0, v27
	v_cmp_gt_f32_e64 s[12:13], v4, v17
	s_and_b64 s[10:11], s[10:11], s[12:13]
	v_cndmask_b32_e64 v17, v17, v4, s[10:11]
	v_and_b32_e32 v27, 0x20000, v18
	v_cndmask_b32_e64 v26, v26, 16, s[10:11]
; __global__ void __launch_bounds__(512, 2) fwd_kernel(Params p) {
;     ...
;                 unsigned mask = 0u; float tv[4];
; #pragma unroll
;                 for (int k = 0; k < 4; ++k) { float best = -__builtin_inff(); int be = 0;
; #pragma unroll
;                     for (int e = 0; e < NE; ++e) { const bool take = !((mask >> e) & 1u) && lgv[e] > best; best = take ? lgv[e] : best; be = take ? e : be; }
;                     mask |= 1u << be; tv[k] = best; te[k] = be; }
	v_cmp_eq_u32_e64 s[10:11], 0, v27
	v_cmp_gt_f32_e64 s[12:13], v0, v17
	s_and_b64 s[10:11], s[10:11], s[12:13]
	v_cndmask_b32_e64 v17, v17, v0, s[10:11]
	v_and_b32_e32 v27, 0x40000, v18
	v_cndmask_b32_e64 v26, v26, 17, s[10:11]
	v_cmp_eq_u32_e64 s[10:11], 0, v27
	v_cmp_gt_f32_e64 s[12:13], v1, v17
	s_and_b64 s[10:11], s[10:11], s[12:13]
	v_cndmask_b32_e64 v17, v17, v1, s[10:11]
	v_and_b32_e32 v27, 0x80000, v18
	v_cndmask_b32_e64 v26, v26, 18, s[10:11]
	v_cmp_eq_u32_e64 s[10:11], 0, v27
	v_cmp_gt_f32_e64 s[12:13], v33, v17
	s_and_b64 s[10:11], s[10:11], s[12:13]
	v_cndmask_b32_e64 v17, v17, v33, s[10:11]
	v_and_b32_e32 v27, 0x100000, v18
	v_cndmask_b32_e64 v26, v26, 19, s[10:11]
	v_cmp_eq_u32_e64 s[10:11], 0, v27
	v_cmp_gt_f32_e64 s[12:13], v8, v17
	s_and_b64 s[10:11], s[10:11], s[12:13]
	v_cndmask_b32_e64 v17, v17, v8, s[10:11]
	v_and_b32_e32 v27, 0x200000, v18
	v_cndmask_b32_e64 v26, v26, 20, s[10:11]
	v_cmp_eq_u32_e64 s[10:11], 0, v27
	v_cmp_gt_f32_e64 s[12:13], v5, v17
	s_and_b64 s[10:11], s[10:11], s[12:13]
	v_cndmask_b32_e64 v17, v17, v5, s[10:11]
	v_and_b32_e32 v27, 0x400000, v18
	v_cndmask_b32_e64 v26, v26, 21, s[10:11]
	v_cmp_eq_u32_e64 s[10:11], 0, v27
	v_cmp_gt_f32_e64 s[12:13], v9, v17
	s_and_b64 s[10:11], s[10:11], s[12:13]
	v_cndmask_b32_e64 v17, v17, v9, s[10:11]
	v_and_b32_e32 v27, 0x800000, v18
	v_cndmask_b32_e64 v26, v26, 22, s[10:11]
	v_cmp_eq_u32_e64 s[10:11], 0, v27
	v_cmp_gt_f32_e64 s[12:13], v29, v17
	s_and_b64 s[10:11], s[10:11], s[12:13]
	v_cndmask_b32_e64 v17, v17, v29, s[10:11]
	v_and_b32_e32 v27, 0x1000000, v18
	v_cndmask_b32_e64 v26, v26, 23, s[10:11]
	v_cmp_eq_u32_e64 s[10:11], 0, v27
	v_cmp_gt_f32_e64 s[12:13], v13, v17
	s_and_b64 s[10:11], s[10:11], s[12:13]
	v_cndmask_b32_e64 v17, v17, v13, s[10:11]
	v_and_b32_e32 v27, 0x2000000, v18
	v_cndmask_b32_e64 v26, v26, 24, s[10:11]
	v_cmp_eq_u32_e64 s[10:11], 0, v27
	v_cmp_gt_f32_e64 s[12:13], v12, v17
	s_and_b64 s[10:11], s[10:11], s[12:13]
	v_cndmask_b32_e64 v17, v17, v12, s[10:11]
	v_and_b32_e32 v27, 0x4000000, v18
	v_cndmask_b32_e64 v26, v26, 25, s[10:11]
	v_cmp_eq_u32_e64 s[10:11], 0, v27
	v_cmp_gt_f32_e64 s[12:13], v22, v17
	s_and_b64 s[10:11], s[10:11], s[12:13]
	v_cndmask_b32_e64 v17, v17, v22, s[10:11]
	v_and_b32_e32 v27, 0x8000000, v18
	v_cndmask_b32_e64 v26, v26, 26, s[10:11]
	v_cmp_eq_u32_e64 s[10:11], 0, v27
	v_cmp_gt_f32_e64 s[12:13], v25, v17
	s_and_b64 s[10:11], s[10:11], s[12:13]
	v_cndmask_b32_e64 v17, v17, v25, s[10:11]
	v_and_b32_e32 v27, 0x10000000, v18
	v_cndmask_b32_e64 v26, v26, 27, s[10:11]
	v_cmp_eq_u32_e64 s[10:11], 0, v27
	v_cmp_gt_f32_e64 s[12:13], v23, v17
	s_and_b64 s[10:11], s[10:11], s[12:13]
	v_cndmask_b32_e64 v17, v17, v23, s[10:11]
	v_and_b32_e32 v27, 0x20000000, v18
	v_cndmask_b32_e64 v26, v26, 28, s[10:11]
	v_cmp_eq_u32_e64 s[10:11], 0, v27
	v_cmp_gt_f32_e64 s[12:13], v19, v17
	s_and_b64 s[10:11], s[10:11], s[12:13]
	v_cndmask_b32_e64 v17, v17, v19, s[10:11]
	v_and_b32_e32 v27, 2.0, v18
	v_cndmask_b32_e64 v26, v26, 29, s[10:11]
	v_cmp_eq_u32_e64 s[10:11], 0, v27
	v_cmp_gt_f32_e64 s[12:13], v20, v17
	s_and_b64 s[10:11], s[10:11], s[12:13]
	v_cndmask_b32_e64 v27, v17, v20, s[10:11]
	v_cndmask_b32_e64 v26, v26, 30, s[10:11]
	v_cmp_ne_u32_e64 s[10:11], 31, v16
	v_cmp_gt_f32_e64 s[12:13], v21, v27
	s_and_b64 s[10:11], s[10:11], s[12:13]
	v_cndmask_b32_e64 v17, v26, 31, s[10:11]
	v_cndmask_b32_e64 v26, v27, v21, s[10:11]
	v_lshl_or_b32 v27, 1, v17, v18
	v_and_b32_e32 v18, 1, v27
	v_cmp_eq_u32_e64 s[10:11], 1, v18
	s_or_b64 s[10:11], s[10:11], vcc
	v_and_b32_e32 v28, 2, v27
	v_cndmask_b32_e64 v18, v37, v139, s[10:11]
	v_cmp_eq_u32_e64 s[10:11], 0, v28
	v_cmp_gt_f32_e64 s[12:13], v36, v18
	s_and_b64 s[10:11], s[10:11], s[12:13]
	v_cndmask_b32_e64 v18, v18, v36, s[10:11]
	v_and_b32_e32 v30, 4, v27
	v_cndmask_b32_e64 v28, 0, 1, s[10:11]
	v_cmp_eq_u32_e64 s[10:11], 0, v30
	v_cmp_gt_f32_e64 s[12:13], v14, v18
	s_and_b64 s[10:11], s[10:11], s[12:13]
	v_cndmask_b32_e64 v18, v18, v14, s[10:11]
	v_and_b32_e32 v30, 8, v27
	v_cndmask_b32_e64 v28, v28, 2, s[10:11]
	v_cmp_eq_u32_e64 s[10:11], 0, v30
	v_cmp_gt_f32_e64 s[12:13], v15, v18
	s_and_b64 s[10:11], s[10:11], s[12:13]
	v_cndmask_b32_e64 v18, v18, v15, s[10:11]
	v_and_b32_e32 v30, 16, v27
	v_cndmask_b32_e64 v28, v28, 3, s[10:11]
	v_cmp_eq_u32_e64 s[10:11], 0, v30
	v_cmp_gt_f32_e64 s[12:13], v39, v18
	s_and_b64 s[10:11], s[10:11], s[12:13]
	v_cndmask_b32_e64 v18, v18, v39, s[10:11]
	v_and_b32_e32 v30, 32, v27
	v_cndmask_b32_e64 v28, v28, 4, s[10:11]
	v_cmp_eq_u32_e64 s[10:11], 0, v30
	v_cmp_gt_f32_e64 s[12:13], v38, v18
	s_and_b64 s[10:11], s[10:11], s[12:13]
	v_cndmask_b32_e64 v18, v18, v38, s[10:11]
	v_and_b32_e32 v30, 64, v27
	v_cndmask_b32_e64 v28, v28, 5, s[10:11]
	v_cmp_eq_u32_e64 s[10:11], 0, v30
	v_cmp_gt_f32_e64 s[12:13], v10, v18
	s_and_b64 s[10:11], s[10:11], s[12:13]
	v_cndmask_b32_e64 v18, v18, v10, s[10:11]
	v_and_b32_e32 v30, 0x80, v27
	v_cndmask_b32_e64 v28, v28, 6, s[10:11]
	v_cmp_eq_u32_e64 s[10:11], 0, v30
	v_cmp_gt_f32_e64 s[12:13], v11, v18
	s_and_b64 s[10:11], s[10:11], s[12:13]
	v_cndmask_b32_e64 v18, v18, v11, s[10:11]
	v_and_b32_e32 v30, 0x100, v27
	v_cndmask_b32_e64 v28, v28, 7, s[10:11]
	v_cmp_eq_u32_e64 s[10:11], 0, v30
	v_cmp_gt_f32_e64 s[12:13], v41, v18
	s_and_b64 s[10:11], s[10:11], s[12:13]
	v_cndmask_b32_e64 v18, v18, v41, s[10:11]
	v_and_b32_e32 v30, 0x200, v27
	v_cndmask_b32_e64 v28, v28, 8, s[10:11]
	v_cmp_eq_u32_e64 s[10:11], 0, v30
	v_cmp_gt_f32_e64 s[12:13], v40, v18
	s_and_b64 s[10:11], s[10:11], s[12:13]
	v_cndmask_b32_e64 v18, v18, v40, s[10:11]
	v_and_b32_e32 v30, 0x400, v27
	v_cndmask_b32_e64 v28, v28, 9, s[10:11]
	v_cmp_eq_u32_e64 s[10:11], 0, v30
; __global__ void __launch_bounds__(512, 2) fwd_kernel(Params p) {
;     ...
;                 unsigned mask = 0u; float tv[4];
; #pragma unroll
;                 for (int k = 0; k < 4; ++k) { float best = -__builtin_inff(); int be = 0;
; #pragma unroll
;                     for (int e = 0; e < NE; ++e) { const bool take = !((mask >> e) & 1u) && lgv[e] > best; best = take ? lgv[e] : best; be = take ? e : be; }
;                     mask |= 1u << be; tv[k] = best; te[k] = be; }
	v_cmp_gt_f32_e64 s[12:13], v6, v18
	s_and_b64 s[10:11], s[10:11], s[12:13]
	v_cndmask_b32_e64 v18, v18, v6, s[10:11]
	v_and_b32_e32 v30, 0x800, v27
	v_cndmask_b32_e64 v28, v28, 10, s[10:11]
	v_cmp_eq_u32_e64 s[10:11], 0, v30
	v_cmp_gt_f32_e64 s[12:13], v7, v18
	s_and_b64 s[10:11], s[10:11], s[12:13]
	v_cndmask_b32_e64 v18, v18, v7, s[10:11]
	v_and_b32_e32 v30, 0x1000, v27
	v_cndmask_b32_e64 v28, v28, 11, s[10:11]
	v_cmp_eq_u32_e64 s[10:11], 0, v30
	v_cmp_gt_f32_e64 s[12:13], v43, v18
	s_and_b64 s[10:11], s[10:11], s[12:13]
	v_cndmask_b32_e64 v18, v18, v43, s[10:11]
	v_and_b32_e32 v30, 0x2000, v27
	v_cndmask_b32_e64 v28, v28, 12, s[10:11]
	v_cmp_eq_u32_e64 s[10:11], 0, v30
	v_cmp_gt_f32_e64 s[12:13], v42, v18
	s_and_b64 s[10:11], s[10:11], s[12:13]
	v_cndmask_b32_e64 v18, v18, v42, s[10:11]
	v_and_b32_e32 v30, 0x4000, v27
	v_cndmask_b32_e64 v28, v28, 13, s[10:11]
	v_cmp_eq_u32_e64 s[10:11], 0, v30
	v_cmp_gt_f32_e64 s[12:13], v2, v18
	s_and_b64 s[10:11], s[10:11], s[12:13]
	v_cndmask_b32_e64 v18, v18, v2, s[10:11]
	v_and_b32_e32 v30, 0x8000, v27
	v_cndmask_b32_e64 v28, v28, 14, s[10:11]
	v_cmp_eq_u32_e64 s[10:11], 0, v30
	v_cmp_gt_f32_e64 s[12:13], v3, v18
	s_and_b64 s[10:11], s[10:11], s[12:13]
	v_cndmask_b32_e64 v18, v18, v3, s[10:11]
	v_and_b32_e32 v30, 0x10000, v27
	v_cndmask_b32_e64 v28, v28, 15, s[10:11]
	v_cmp_eq_u32_e64 s[10:11], 0, v30
	v_cmp_gt_f32_e64 s[12:13], v4, v18
	s_and_b64 s[10:11], s[10:11], s[12:13]
	v_cndmask_b32_e64 v18, v18, v4, s[10:11]
	v_and_b32_e32 v30, 0x20000, v27
	v_cndmask_b32_e64 v28, v28, 16, s[10:11]
	v_cmp_eq_u32_e64 s[10:11], 0, v30
	v_cmp_gt_f32_e64 s[12:13], v0, v18
	s_and_b64 s[10:11], s[10:11], s[12:13]
	v_cndmask_b32_e64 v18, v18, v0, s[10:11]
	v_and_b32_e32 v30, 0x40000, v27
	v_cndmask_b32_e64 v28, v28, 17, s[10:11]
	v_cmp_eq_u32_e64 s[10:11], 0, v30
	v_cmp_gt_f32_e64 s[12:13], v1, v18
	s_and_b64 s[10:11], s[10:11], s[12:13]
	v_cndmask_b32_e64 v18, v18, v1, s[10:11]
	v_and_b32_e32 v30, 0x80000, v27
	v_cndmask_b32_e64 v28, v28, 18, s[10:11]
	v_cmp_eq_u32_e64 s[10:11], 0, v30
	v_cmp_gt_f32_e64 s[12:13], v33, v18
	s_and_b64 s[10:11], s[10:11], s[12:13]
	v_cndmask_b32_e64 v18, v18, v33, s[10:11]
	v_and_b32_e32 v30, 0x100000, v27
	v_cndmask_b32_e64 v28, v28, 19, s[10:11]
	v_cmp_eq_u32_e64 s[10:11], 0, v30
	v_cmp_gt_f32_e64 s[12:13], v8, v18
	s_and_b64 s[10:11], s[10:11], s[12:13]
	v_cndmask_b32_e64 v18, v18, v8, s[10:11]
	v_and_b32_e32 v30, 0x200000, v27
	v_cndmask_b32_e64 v28, v28, 20, s[10:11]
	v_cmp_eq_u32_e64 s[10:11], 0, v30
	v_cmp_gt_f32_e64 s[12:13], v5, v18
	s_and_b64 s[10:11], s[10:11], s[12:13]
	v_cndmask_b32_e64 v18, v18, v5, s[10:11]
	v_and_b32_e32 v30, 0x400000, v27
	v_cndmask_b32_e64 v28, v28, 21, s[10:11]
	v_cmp_eq_u32_e64 s[10:11], 0, v30
	v_cmp_gt_f32_e64 s[12:13], v9, v18
	s_and_b64 s[10:11], s[10:11], s[12:13]
	v_cndmask_b32_e64 v18, v18, v9, s[10:11]
	v_and_b32_e32 v30, 0x800000, v27
	v_cndmask_b32_e64 v28, v28, 22, s[10:11]
	v_cmp_eq_u32_e64 s[10:11], 0, v30
	v_cmp_gt_f32_e64 s[12:13], v29, v18
	s_and_b64 s[10:11], s[10:11], s[12:13]
	v_cndmask_b32_e64 v18, v18, v29, s[10:11]
	v_and_b32_e32 v30, 0x1000000, v27
	v_cndmask_b32_e64 v28, v28, 23, s[10:11]
	v_cmp_eq_u32_e64 s[10:11], 0, v30
	v_cmp_gt_f32_e64 s[12:13], v13, v18
	s_and_b64 s[10:11], s[10:11], s[12:13]
	v_cndmask_b32_e64 v18, v18, v13, s[10:11]
	v_and_b32_e32 v30, 0x2000000, v27
	v_cndmask_b32_e64 v28, v28, 24, s[10:11]
	v_cmp_eq_u32_e64 s[10:11], 0, v30
	v_cmp_gt_f32_e64 s[12:13], v12, v18
	s_and_b64 s[10:11], s[10:11], s[12:13]
	v_cndmask_b32_e64 v18, v18, v12, s[10:11]
	v_and_b32_e32 v30, 0x4000000, v27
	v_cndmask_b32_e64 v28, v28, 25, s[10:11]
	v_cmp_eq_u32_e64 s[10:11], 0, v30
	v_cmp_gt_f32_e64 s[12:13], v22, v18
	s_and_b64 s[10:11], s[10:11], s[12:13]
	v_cndmask_b32_e64 v18, v18, v22, s[10:11]
	v_and_b32_e32 v30, 0x8000000, v27
	v_cndmask_b32_e64 v28, v28, 26, s[10:11]
	v_cmp_eq_u32_e64 s[10:11], 0, v30
	v_cmp_gt_f32_e64 s[12:13], v25, v18
	s_and_b64 s[10:11], s[10:11], s[12:13]
	v_cndmask_b32_e64 v18, v18, v25, s[10:11]
	v_and_b32_e32 v30, 0x10000000, v27
	v_cndmask_b32_e64 v28, v28, 27, s[10:11]
	v_cmp_eq_u32_e64 s[10:11], 0, v30
	v_cmp_gt_f32_e64 s[12:13], v23, v18
	s_and_b64 s[10:11], s[10:11], s[12:13]
	v_cndmask_b32_e64 v18, v18, v23, s[10:11]
	v_and_b32_e32 v30, 0x20000000, v27
	v_cndmask_b32_e64 v28, v28, 28, s[10:11]
	v_cmp_eq_u32_e64 s[10:11], 0, v30
	v_cmp_gt_f32_e64 s[12:13], v19, v18
	s_and_b64 s[10:11], s[10:11], s[12:13]
	v_cndmask_b32_e64 v18, v18, v19, s[10:11]
	v_and_b32_e32 v30, 2.0, v27
	v_cndmask_b32_e64 v28, v28, 29, s[10:11]
	v_cmp_eq_u32_e64 s[10:11], 0, v30
	v_cmp_gt_f32_e64 s[12:13], v20, v18
	s_and_b64 s[10:11], s[10:11], s[12:13]
	v_cndmask_b32_e64 v30, v18, v20, s[10:11]
	v_cndmask_b32_e64 v28, v28, 30, s[10:11]
	v_cmp_lt_i32_e64 s[10:11], -1, v27
	v_cmp_gt_f32_e64 s[12:13], v21, v30
	s_and_b64 s[10:11], s[10:11], s[12:13]
	v_cndmask_b32_e64 v18, v28, 31, s[10:11]
	v_cndmask_b32_e64 v28, v30, v21, s[10:11]
	v_lshlrev_b32_e64 v30, v18, 1
	v_or_b32_e32 v31, v30, v27
	v_and_b32_e32 v32, 1, v31
	v_cmp_eq_u32_e64 s[10:11], 1, v32
	s_or_b64 vcc, s[10:11], vcc
	v_cndmask_b32_e32 v32, v37, v139, vcc
	v_bitop3_b32 v37, v30, 2, v27 bitop3:0xc8
	v_cmp_eq_u32_e32 vcc, 0, v37
	v_cmp_gt_f32_e64 s[10:11], v36, v32
	s_and_b64 vcc, vcc, s[10:11]
	v_cndmask_b32_e32 v32, v32, v36, vcc
	v_bitop3_b32 v36, v30, 4, v27 bitop3:0xc8
	v_cndmask_b32_e64 v37, 0, 1, vcc
	v_cmp_eq_u32_e32 vcc, 0, v36
	v_cmp_gt_f32_e64 s[10:11], v14, v32
	s_and_b64 vcc, vcc, s[10:11]
	v_cndmask_b32_e32 v14, v32, v14, vcc
	v_bitop3_b32 v32, v30, 8, v27 bitop3:0xc8
	v_cndmask_b32_e64 v36, v37, 2, vcc
	v_cmp_eq_u32_e32 vcc, 0, v32
; __global__ void __launch_bounds__(512, 2) fwd_kernel(Params p) {
;     ...
;                 for (int k = 0; k < 4; ++k) { float best = -__builtin_inff(); int be = 0;
; #pragma unroll
;                     for (int e = 0; e < NE; ++e) { const bool take = !((mask >> e) & 1u) && lgv[e] > best; best = take ? lgv[e] : best; be = take ? e : be; }
;                     mask |= 1u << be; tv[k] = best; te[k] = be; }
;                 float ex[4], sum = 0.f;
; #pragma unroll
;                 for (int k = 0; k < 4; ++k) { ex[k] = __expf(tv[k] - tv[0]); sum += ex[k]; }
;                 const float inv = 1.0f / sum;
; #pragma unroll
;                 for (int k = 0; k < 4; ++k) { lrk[tid * 4 + k] = atomicAdd((int*)&hist[te[k]], 1); tok_e[tok * 4 + k] = te[k]; tok_w[tok * 4 + k] = ex[k] * inv; }
	v_cmp_gt_f32_e64 s[10:11], v15, v14
	s_and_b64 vcc, vcc, s[10:11]
	v_cndmask_b32_e32 v14, v14, v15, vcc
	v_bitop3_b32 v15, v30, 16, v27 bitop3:0xc8
	v_cndmask_b32_e64 v32, v36, 3, vcc
	v_cmp_eq_u32_e32 vcc, 0, v15
	v_cmp_gt_f32_e64 s[10:11], v39, v14
	s_and_b64 vcc, vcc, s[10:11]
	v_cndmask_b32_e64 v15, v32, 4, vcc
	v_cndmask_b32_e32 v14, v14, v39, vcc
	v_bitop3_b32 v32, v30, 32, v27 bitop3:0xc8
	v_cmp_eq_u32_e32 vcc, 0, v32
	v_cmp_gt_f32_e64 s[10:11], v38, v14
	s_and_b64 vcc, vcc, s[10:11]
	v_cndmask_b32_e32 v14, v14, v38, vcc
	v_bitop3_b32 v32, v30, 64, v27 bitop3:0xc8
	v_cndmask_b32_e64 v15, v15, 5, vcc
	v_cmp_eq_u32_e32 vcc, 0, v32
	v_cmp_gt_f32_e64 s[10:11], v10, v14
	s_and_b64 vcc, vcc, s[10:11]
	v_cndmask_b32_e32 v10, v14, v10, vcc
	v_bitop3_b32 v14, v30, s0, v27 bitop3:0xc8
	v_cndmask_b32_e64 v15, v15, 6, vcc
	v_cmp_eq_u32_e32 vcc, 0, v14
	v_cmp_gt_f32_e64 s[10:11], v11, v10
	s_and_b64 vcc, vcc, s[10:11]
	s_movk_i32 s0, 0x100
	v_cndmask_b32_e32 v10, v10, v11, vcc
	v_bitop3_b32 v11, v30, s0, v27 bitop3:0xc8
	v_cndmask_b32_e64 v14, v15, 7, vcc
	v_cmp_eq_u32_e32 vcc, 0, v11
	v_cmp_gt_f32_e64 s[10:11], v41, v10
	s_and_b64 vcc, vcc, s[10:11]
	s_movk_i32 s0, 0x200
	v_cndmask_b32_e64 v11, v14, 8, vcc
	v_cndmask_b32_e32 v10, v10, v41, vcc
	v_bitop3_b32 v14, v30, s0, v27 bitop3:0xc8
	v_cmp_eq_u32_e32 vcc, 0, v14
	v_cmp_gt_f32_e64 s[10:11], v40, v10
	s_and_b64 vcc, vcc, s[10:11]
	s_movk_i32 s0, 0x400
	v_cndmask_b32_e32 v10, v10, v40, vcc
	v_bitop3_b32 v14, v30, s0, v27 bitop3:0xc8
	v_cndmask_b32_e64 v11, v11, 9, vcc
	v_cmp_eq_u32_e32 vcc, 0, v14
	v_cmp_gt_f32_e64 s[10:11], v6, v10
	s_and_b64 vcc, vcc, s[10:11]
	v_cndmask_b32_e32 v6, v10, v6, vcc
	v_bitop3_b32 v10, v30, s59, v27 bitop3:0xc8
	v_cndmask_b32_e64 v11, v11, 10, vcc
	v_cmp_eq_u32_e32 vcc, 0, v10
	v_cmp_gt_f32_e64 s[10:11], v7, v6
	s_and_b64 vcc, vcc, s[10:11]
	v_cndmask_b32_e32 v6, v6, v7, vcc
	v_bitop3_b32 v7, v30, s60, v27 bitop3:0xc8
	v_cndmask_b32_e64 v10, v11, 11, vcc
	v_cmp_eq_u32_e32 vcc, 0, v7
	v_cmp_gt_f32_e64 s[10:11], v43, v6
	s_and_b64 vcc, vcc, s[10:11]
	v_cndmask_b32_e64 v7, v10, 12, vcc
	v_cndmask_b32_e32 v6, v6, v43, vcc
	v_bitop3_b32 v10, v30, s61, v27 bitop3:0xc8
	v_cmp_eq_u32_e32 vcc, 0, v10
	v_cmp_gt_f32_e64 s[10:11], v42, v6
	s_and_b64 vcc, vcc, s[10:11]
	s_movk_i32 s0, 0x4000
	v_cndmask_b32_e32 v6, v6, v42, vcc
	v_bitop3_b32 v10, v30, s0, v27 bitop3:0xc8
	v_cndmask_b32_e64 v7, v7, 13, vcc
	v_cmp_eq_u32_e32 vcc, 0, v10
	v_cmp_gt_f32_e64 s[10:11], v2, v6
	s_and_b64 vcc, vcc, s[10:11]
	v_cndmask_b32_e32 v2, v6, v2, vcc
	v_bitop3_b32 v6, v30, s62, v27 bitop3:0xc8
	v_cndmask_b32_e64 v7, v7, 14, vcc
	v_cmp_eq_u32_e32 vcc, 0, v6
	v_cmp_gt_f32_e64 s[10:11], v3, v2
	s_and_b64 vcc, vcc, s[10:11]
	v_cndmask_b32_e32 v2, v2, v3, vcc
	v_bitop3_b32 v3, v30, s63, v27 bitop3:0xc8
	v_cndmask_b32_e64 v6, v7, 15, vcc
	v_cmp_eq_u32_e32 vcc, 0, v3
	v_cmp_gt_f32_e64 s[10:11], v4, v2
	s_and_b64 vcc, vcc, s[10:11]
	v_cndmask_b32_e32 v2, v2, v4, vcc
	v_bitop3_b32 v4, v30, s64, v27 bitop3:0xc8
	v_cndmask_b32_e64 v3, v6, 16, vcc
	v_cmp_eq_u32_e32 vcc, 0, v4
	v_cmp_gt_f32_e64 s[10:11], v0, v2
	s_and_b64 vcc, vcc, s[10:11]
	v_cndmask_b32_e32 v0, v2, v0, vcc
	v_bitop3_b32 v2, v30, s65, v27 bitop3:0xc8
	v_cndmask_b32_e64 v3, v3, 17, vcc
	v_cmp_eq_u32_e32 vcc, 0, v2
	v_cmp_gt_f32_e64 s[10:11], v1, v0
	s_and_b64 vcc, vcc, s[10:11]
	v_cndmask_b32_e32 v0, v0, v1, vcc
	v_bitop3_b32 v1, v30, s66, v27 bitop3:0xc8
	v_cndmask_b32_e64 v2, v3, 18, vcc
	v_cmp_eq_u32_e32 vcc, 0, v1
	v_cmp_gt_f32_e64 s[10:11], v33, v0
	s_and_b64 vcc, vcc, s[10:11]
	v_cndmask_b32_e64 v1, v2, 19, vcc
	v_cndmask_b32_e32 v0, v0, v33, vcc
	v_bitop3_b32 v2, v30, s67, v27 bitop3:0xc8
	v_cmp_eq_u32_e32 vcc, 0, v2
	v_cmp_gt_f32_e64 s[10:11], v8, v0
	s_and_b64 vcc, vcc, s[10:11]
	v_cndmask_b32_e32 v0, v0, v8, vcc
	v_bitop3_b32 v2, v30, s68, v27 bitop3:0xc8
	v_cndmask_b32_e64 v1, v1, 20, vcc
	v_cmp_eq_u32_e32 vcc, 0, v2
	v_cmp_gt_f32_e64 s[10:11], v5, v0
	s_and_b64 vcc, vcc, s[10:11]
	v_cndmask_b32_e32 v0, v0, v5, vcc
	v_bitop3_b32 v2, v30, s69, v27 bitop3:0xc8
	v_cndmask_b32_e64 v1, v1, 21, vcc
	v_cmp_eq_u32_e32 vcc, 0, v2
	v_cmp_gt_f32_e64 s[10:11], v9, v0
	s_and_b64 vcc, vcc, s[10:11]
	v_cndmask_b32_e32 v0, v0, v9, vcc
	v_bitop3_b32 v2, v30, s57, v27 bitop3:0xc8
	v_cndmask_b32_e64 v1, v1, 22, vcc
	v_cmp_eq_u32_e32 vcc, 0, v2
	v_cmp_gt_f32_e64 s[10:11], v29, v0
	s_and_b64 vcc, vcc, s[10:11]
	v_cndmask_b32_e32 v0, v0, v29, vcc
	v_bitop3_b32 v2, v30, s70, v27 bitop3:0xc8
	v_cndmask_b32_e64 v1, v1, 23, vcc
	v_cmp_eq_u32_e32 vcc, 0, v2
	v_cmp_gt_f32_e64 s[10:11], v13, v0
	s_and_b64 vcc, vcc, s[10:11]
	v_cndmask_b32_e32 v0, v0, v13, vcc
	v_bitop3_b32 v2, v30, s71, v27 bitop3:0xc8
	v_cndmask_b32_e64 v1, v1, 24, vcc
	v_cmp_eq_u32_e32 vcc, 0, v2
	v_cmp_gt_f32_e64 s[10:11], v12, v0
	s_and_b64 vcc, vcc, s[10:11]
	v_cndmask_b32_e32 v0, v0, v12, vcc
	v_bitop3_b32 v2, v30, s72, v27 bitop3:0xc8
	v_cndmask_b32_e64 v1, v1, 25, vcc
	v_cmp_eq_u32_e32 vcc, 0, v2
	v_cmp_gt_f32_e64 s[10:11], v22, v0
	s_and_b64 vcc, vcc, s[10:11]
	v_cndmask_b32_e32 v0, v0, v22, vcc
	v_bitop3_b32 v2, v30, s73, v27 bitop3:0xc8
	v_cndmask_b32_e64 v1, v1, 26, vcc
	v_cmp_eq_u32_e32 vcc, 0, v2
	v_cmp_gt_f32_e64 s[10:11], v25, v0
	s_and_b64 vcc, vcc, s[10:11]
	v_cndmask_b32_e32 v0, v0, v25, vcc
	v_bitop3_b32 v2, v30, s74, v27 bitop3:0xc8
	v_cndmask_b32_e64 v1, v1, 27, vcc
	v_cmp_eq_u32_e32 vcc, 0, v2
	v_cmp_gt_f32_e64 s[10:11], v23, v0
	s_and_b64 vcc, vcc, s[10:11]
	v_cndmask_b32_e32 v0, v0, v23, vcc
	v_bitop3_b32 v2, v30, s75, v27 bitop3:0xc8
	v_cndmask_b32_e64 v1, v1, 28, vcc
	v_cmp_eq_u32_e32 vcc, 0, v2
	v_cmp_gt_f32_e64 s[10:11], v19, v0
	s_and_b64 vcc, vcc, s[10:11]
	v_cndmask_b32_e32 v0, v0, v19, vcc
	v_bitop3_b32 v2, v30, 2.0, v27 bitop3:0xc8
	v_cndmask_b32_e64 v1, v1, 29, vcc
	v_cmp_eq_u32_e32 vcc, 0, v2
	v_cmp_gt_f32_e64 s[10:11], v20, v0
	s_and_b64 vcc, vcc, s[10:11]
	v_cndmask_b32_e32 v0, v0, v20, vcc
	v_cndmask_b32_e64 v1, v1, 30, vcc
	v_cmp_lt_i32_e32 vcc, -1, v31
	v_cmp_gt_f32_e64 s[10:11], v21, v0
	s_and_b64 vcc, vcc, s[10:11]
	v_cndmask_b32_e64 v19, v1, 31, vcc
	v_sub_f32_e32 v1, v24, v24
	v_sub_f32_e32 v2, v26, v24
	v_mul_f32_e32 v1, 0x3fb8aa3b, v1
	v_mul_f32_e32 v2, 0x3fb8aa3b, v2
	v_cndmask_b32_e32 v0, v0, v21, vcc
	v_exp_f32_e32 v6, v1
	v_exp_f32_e32 v7, v2
	v_sub_f32_e32 v2, v28, v24
	v_mul_f32_e32 v2, 0x3fb8aa3b, v2
	v_sub_f32_e32 v0, v0, v24
	v_exp_f32_e32 v8, v2
	v_mul_f32_e32 v0, 0x3fb8aa3b, v0
	v_exp_f32_e32 v9, v0
	v_add_f32_e32 v1, 0, v6
	v_add_f32_e32 v1, v1, v7
	v_add_f32_e32 v1, v1, v8
	v_add_f32_e32 v0, v1, v9
	v_div_scale_f32 v1, s[0:1], v0, v0, 1.0
	v_rcp_f32_e32 v2, v1
	v_add_u32_e32 v11, 0, v134
	v_fma_f32 v3, -v1, v2, 1.0
	v_fmac_f32_e32 v2, v3, v2
	v_div_scale_f32 v3, vcc, 1.0, v0, 1.0
	v_mul_f32_e32 v4, v3, v2
	v_fma_f32 v5, -v1, v4, v3
	v_fmac_f32_e32 v4, v5, v2
	v_fma_f32 v1, -v1, v4, v3
	v_div_fmas_f32 v1, v1, v2, v4
	v_div_fixup_f32 v10, v1, v0, 1.0
	v_lshl_add_u32 v1, v16, 2, 0
	ds_add_rtn_u32 v1, v1, v138 offset:53760
	v_lshlrev_b32_e32 v0, 2, v34
	s_waitcnt lgkmcnt(0)
; __global__ void __launch_bounds__(512, 2) fwd_kernel(Params p) {
;     ...
;                 for (int k = 0; k < 4; ++k) { lrk[tid * 4 + k] = atomicAdd((int*)&hist[te[k]], 1); tok_e[tok * 4 + k] = te[k]; tok_w[tok * 4 + k] = ex[k] * inv; }
	ds_write_b32 v11, v1 offset:40960
	v_ashrrev_i32_e32 v1, 31, v0
	v_lshlrev_b64 v[2:3], 2, v[0:1]
	v_lshl_add_u64 v[4:5], s[16:17], 0, v[2:3]
	v_mul_f32_e32 v1, v10, v6
	v_mov_b32_e32 v240, v1
	v_lshl_add_u64 v[2:3], s[42:43], 0, v[2:3]
	global_store_dword v[2:3], v1, off
	v_lshl_add_u32 v1, v17, 2, 0
	ds_add_rtn_u32 v1, v1, v138 offset:53760
	v_or_b32_e32 v2, 1, v0
	v_ashrrev_i32_e32 v3, 31, v2
	v_mul_f32_e32 v0, v10, v7
	v_lshl_add_u64 v[6:7], v[2:3], 2, s[42:43]
	s_waitcnt lgkmcnt(0)
	ds_write_b32 v11, v1 offset:40964
	v_lshl_add_u32 v1, v18, 2, 0
	ds_add_rtn_u32 v1, v1, v138 offset:53760
	v_lshl_add_u32 v2, v19, 2, 0
	s_waitcnt lgkmcnt(0)
	ds_write_b32 v11, v1 offset:40968
	ds_add_rtn_u32 v2, v2, v138 offset:53760
	v_mul_f32_e32 v1, v10, v8
	global_store_dwordx4 v[4:5], v[16:19], off
	s_waitcnt lgkmcnt(0)
	ds_write_b32 v11, v2 offset:40972
	v_mul_f32_e32 v2, v10, v9
	v_mov_b32_e32 v241, v0
	v_mov_b32_e32 v242, v1
	v_mov_b32_e32 v243, v2
	global_store_dwordx3 v[6:7], v[0:2], off
